# baseline (speedup 1.0000x reference)
_Z11prep_kernelPKfS0_PKiPDF16_S3_PfS4_:
	s_lshl_b32 s14, s2, 2
	v_lshrrev_b32_e32 v1, 8, v0
	v_or_b32_e32 v5, s14, v1
	s_movk_i32 s2, 0xff
	v_and_b32_e32 v4, 0xff, v0
	v_cmp_lt_i32_e32 vcc, s2, v5
	s_and_saveexec_b64 s[2:3], vcc
	s_xor_b64 s[2:3], exec, s[2:3]
	s_cbranch_execz .LBB0_5
	v_readfirstlane_b32 s15, v0
	s_bitcmp1_b32 s15, 7
	s_cbranch_scc1 .LBB0_7
	s_load_dwordx4 s[8:11], s[0:1], 0x0
	s_load_dwordx4 s[4:7], s[0:1], 0x18
	v_add_u32_e32 v34, 0xffffff00, v5
	v_mov_b32_e32 v35, 0
	v_lshlrev_b64 v[32:33], 11, v[34:35]
	v_lshl_or_b32 v32, v4, 3, v32
	v_lshlrev_b64 v[0:1], 2, v[32:33]
	s_waitcnt lgkmcnt(0)
	s_cmp_lg_u32 s14, 0x100
	s_cbranch_scc1 .Lprep_noflag
	s_cmp_gt_u32 s15, 63
	s_cbranch_scc1 .Lprep_noflag
	s_add_u32 s16, s4, 0x3c08000
	s_addc_u32 s17, s5, 0
	v_lshlrev_b32_e32 v6, 2, v4
	v_mov_b32_e32 v7, 0
	v_mov_b32_e32 v8, s8
	v_mov_b32_e32 v9, s9
	v_mov_b32_e32 v10, s10
	v_mov_b32_e32 v11, s11
	global_store_dword v6, v7, s[16:17]
	global_store_dword v6, v7, s[16:17] offset:256
	global_store_dword v6, v7, s[16:17] offset:512
	global_store_dword v6, v7, s[16:17] offset:768
	global_store_dwordx4 v7, v[8:11], s[16:17] offset:1024

.LBB1_9:
	s_cmp_lt_i32 s56, 10
	s_cbranch_scc1 .Lqkv_nopoll
	s_cmp_gt_i32 s56, 24
	s_cbranch_scc1 .Lqkv_nopoll
	s_bitcmp1_b32 s56, 1
	s_cbranch_scc0 .Lqkv_chk
	s_sub_u32 s82, s56, 10
	s_lshl_b32 s82, s82, 6
	v_add_u32_e32 v242, s82, v241
	global_load_dword v240, v242, s[80:81] sc1
	s_branch .Lqkv_nopoll
.Lqkv_chk:
	s_mov_b32 s83, 0
	s_branch .Lqkv_check
.Lqkv_poll:
	global_load_dword v240, v242, s[80:81] sc1
	s_waitcnt vmcnt(0)

.LBB1_30:
	s_and_b64 vcc, exec, s[4:5]
	s_cbranch_vccz .LBB1_41
	s_load_dwordx4 s[44:47], s[0:1], 0x0
	s_load_dwordx2 s[48:49], s[0:1], 0x20
	s_add_i32 s50, s2, 0xffffff40
	v_and_b32_e32 v1, 31, v0
	v_lshrrev_b32_e32 v2, 5, v0
	v_lshlrev_b32_e32 v3, 5, v1
	v_lshl_add_u32 v3, v2, 13, v3
	v_add_u32_e32 v3, 0x1000, v3
	v_lshlrev_b32_e32 v4, 4, v1
	v_lshl_add_u32 v4, v2, 12, v4
	v_add_u32_e32 v4, 0x800, v4
	s_waitcnt lgkmcnt(0)
	s_add_u32 s48, s48, 0x408000
	s_addc_u32 s49, s49, 0
	s_load_dwordx4 s[52:55], s[48:49], 0x400
	s_lshl_b32 s51, s50, 18
	s_add_u32 s44, s44, s51
	s_addc_u32 s45, s45, 0
	s_mul_i32 s51, s50, 0x30000
	s_add_u32 s46, s46, s51
	s_addc_u32 s47, s47, 0
	s_waitcnt lgkmcnt(0)
	s_lshl_b32 s51, s50, 19
	s_add_u32 s52, s52, s51
	s_addc_u32 s53, s53, 0
	s_mul_i32 s51, s50, 0x60000
	s_add_u32 s54, s54, s51
	s_addc_u32 s55, s55, 0
	v_cmp_eq_u32_e64 s[78:79], 0, v0
	v_mov_b32_e32 v5, 1
	v_mov_b32_e32 v6, s50
	v_lshlrev_b32_e32 v6, 2, v6
	s_add_u32 s58, s52, 0x0
	s_addc_u32 s59, s53, 0
	global_load_dwordx4 v[16:19], v3, s[58:59] nt
	global_load_dwordx4 v[20:23], v3, s[58:59] offset:16 nt
	s_add_u32 s58, s52, 0x20000
	s_addc_u32 s59, s53, 0
	global_load_dwordx4 v[24:27], v3, s[58:59] nt
	global_load_dwordx4 v[28:31], v3, s[58:59] offset:16 nt
	s_add_u32 s58, s52, 0x40000
	s_addc_u32 s59, s53, 0
	global_load_dwordx4 v[32:35], v3, s[58:59] nt
	global_load_dwordx4 v[36:39], v3, s[58:59] offset:16 nt
	s_add_u32 s58, s52, 0x60000
	s_addc_u32 s59, s53, 0
	global_load_dwordx4 v[40:43], v3, s[58:59] nt
	global_load_dwordx4 v[44:47], v3, s[58:59] offset:16 nt
	s_add_u32 s58, s54, 0x0
	s_addc_u32 s59, s55, 0
	global_load_dwordx4 v[48:51], v3, s[58:59] nt
	global_load_dwordx4 v[52:55], v3, s[58:59] offset:16 nt
	s_add_u32 s58, s54, 0x20000
	s_addc_u32 s59, s55, 0
	global_load_dwordx4 v[56:59], v3, s[58:59] nt
	global_load_dwordx4 v[60:63], v3, s[58:59] offset:16 nt
	s_add_u32 s58, s54, 0x40000
	s_addc_u32 s59, s55, 0
	global_load_dwordx4 v[64:67], v3, s[58:59] nt
	global_load_dwordx4 v[68:71], v3, s[58:59] offset:16 nt
	s_add_u32 s58, s52, 0x400
	s_addc_u32 s59, s53, 0
	global_load_dwordx4 v[72:75], v3, s[58:59] nt
	global_load_dwordx4 v[76:79], v3, s[58:59] offset:16 nt
	s_add_u32 s58, s52, 0x20400
	s_addc_u32 s59, s53, 0
	global_load_dwordx4 v[80:83], v3, s[58:59] nt
	global_load_dwordx4 v[84:87], v3, s[58:59] offset:16 nt
	s_add_u32 s58, s52, 0x40400
	s_addc_u32 s59, s53, 0
	global_load_dwordx4 v[88:91], v3, s[58:59] nt
	global_load_dwordx4 v[92:95], v3, s[58:59] offset:16 nt
	s_add_u32 s58, s52, 0x60400
	s_addc_u32 s59, s53, 0
	global_load_dwordx4 v[96:99], v3, s[58:59] nt
	global_load_dwordx4 v[100:103], v3, s[58:59] offset:16 nt
	s_add_u32 s58, s54, 0x400
	s_addc_u32 s59, s55, 0
	global_load_dwordx4 v[104:107], v3, s[58:59] nt
	global_load_dwordx4 v[108:111], v3, s[58:59] offset:16 nt
	s_add_u32 s58, s54, 0x20400
	s_addc_u32 s59, s55, 0
	global_load_dwordx4 v[112:115], v3, s[58:59] nt
	global_load_dwordx4 v[116:119], v3, s[58:59] offset:16 nt
	s_add_u32 s58, s54, 0x40400
	s_addc_u32 s59, s55, 0
	global_load_dwordx4 v[120:123], v3, s[58:59] nt
	global_load_dwordx4 v[124:127], v3, s[58:59] offset:16 nt
	s_waitcnt vmcnt(26)
	v_cvt_pk_f16_f32 v16, v16, v17
	v_cvt_pk_f16_f32 v17, v18, v19
	v_cvt_pk_f16_f32 v18, v20, v21
	v_cvt_pk_f16_f32 v19, v22, v23
	s_add_u32 s76, s44, 0x0
	s_addc_u32 s77, s45, 0
	global_store_dwordx4 v4, v[16:19], s[76:77] sc1
	s_waitcnt vmcnt(25)
	v_cvt_pk_f16_f32 v24, v24, v25
	v_cvt_pk_f16_f32 v25, v26, v27
	v_cvt_pk_f16_f32 v26, v28, v29
	v_cvt_pk_f16_f32 v27, v30, v31
	s_add_u32 s76, s44, 0x10000
	s_addc_u32 s77, s45, 0
	global_store_dwordx4 v4, v[24:27], s[76:77] sc1
	s_waitcnt vmcnt(24)
	v_cvt_pk_f16_f32 v32, v32, v33
	v_cvt_pk_f16_f32 v33, v34, v35
	v_cvt_pk_f16_f32 v34, v36, v37
	v_cvt_pk_f16_f32 v35, v38, v39
	s_add_u32 s76, s44, 0x20000
	s_addc_u32 s77, s45, 0
	global_store_dwordx4 v4, v[32:35], s[76:77] sc1
	s_waitcnt vmcnt(23)
	v_cvt_pk_f16_f32 v40, v40, v41
	v_cvt_pk_f16_f32 v41, v42, v43
	v_cvt_pk_f16_f32 v42, v44, v45
	v_cvt_pk_f16_f32 v43, v46, v47
	s_add_u32 s76, s44, 0x30000
	s_addc_u32 s77, s45, 0
	global_store_dwordx4 v4, v[40:43], s[76:77] sc1
	s_waitcnt vmcnt(22)
	v_cvt_pk_f16_f32 v48, v48, v49
	v_cvt_pk_f16_f32 v49, v50, v51
	v_cvt_pk_f16_f32 v50, v52, v53
	v_cvt_pk_f16_f32 v51, v54, v55
	s_add_u32 s76, s46, 0x0
	s_addc_u32 s77, s47, 0
	global_store_dwordx4 v4, v[48:51], s[76:77] sc1
	s_waitcnt vmcnt(21)
	v_cvt_pk_f16_f32 v56, v56, v57
	v_cvt_pk_f16_f32 v57, v58, v59
	v_cvt_pk_f16_f32 v58, v60, v61
	v_cvt_pk_f16_f32 v59, v62, v63
	s_add_u32 s76, s46, 0x10000
	s_addc_u32 s77, s47, 0
	global_store_dwordx4 v4, v[56:59], s[76:77] sc1
	s_waitcnt vmcnt(20)
	v_cvt_pk_f16_f32 v64, v64, v65
	v_cvt_pk_f16_f32 v65, v66, v67
	v_cvt_pk_f16_f32 v66, v68, v69
	v_cvt_pk_f16_f32 v67, v70, v71
	s_add_u32 s76, s46, 0x20000
	s_addc_u32 s77, s47, 0
	global_store_dwordx4 v4, v[64:67], s[76:77] sc1
	s_add_u32 s58, s52, 0x800
	s_addc_u32 s59, s53, 0
	global_load_dwordx4 v[16:19], v3, s[58:59] nt
	global_load_dwordx4 v[20:23], v3, s[58:59] offset:16 nt
	s_add_u32 s58, s52, 0x20800
	s_addc_u32 s59, s53, 0
	global_load_dwordx4 v[24:27], v3, s[58:59] nt
	global_load_dwordx4 v[28:31], v3, s[58:59] offset:16 nt
	s_add_u32 s58, s52, 0x40800
	s_addc_u32 s59, s53, 0
	global_load_dwordx4 v[32:35], v3, s[58:59] nt
	global_load_dwordx4 v[36:39], v3, s[58:59] offset:16 nt
	s_add_u32 s58, s52, 0x60800
	s_addc_u32 s59, s53, 0
	global_load_dwordx4 v[40:43], v3, s[58:59] nt
	global_load_dwordx4 v[44:47], v3, s[58:59] offset:16 nt
	s_add_u32 s58, s54, 0x800
	s_addc_u32 s59, s55, 0
	global_load_dwordx4 v[48:51], v3, s[58:59] nt
	global_load_dwordx4 v[52:55], v3, s[58:59] offset:16 nt
	s_add_u32 s58, s54, 0x20800
	s_addc_u32 s59, s55, 0
	global_load_dwordx4 v[56:59], v3, s[58:59] nt
	global_load_dwordx4 v[60:63], v3, s[58:59] offset:16 nt
	s_add_u32 s58, s54, 0x40800
	s_addc_u32 s59, s55, 0
	global_load_dwordx4 v[64:67], v3, s[58:59] nt
	global_load_dwordx4 v[68:71], v3, s[58:59] offset:16 nt
	s_waitcnt vmcnt(33)
	v_cvt_pk_f16_f32 v72, v72, v73
	v_cvt_pk_f16_f32 v73, v74, v75
	v_cvt_pk_f16_f32 v74, v76, v77
	v_cvt_pk_f16_f32 v75, v78, v79
	s_add_u32 s76, s44, 0x200
	s_addc_u32 s77, s45, 0
	global_store_dwordx4 v4, v[72:75], s[76:77] sc1
	s_waitcnt vmcnt(32)
	v_cvt_pk_f16_f32 v80, v80, v81
	v_cvt_pk_f16_f32 v81, v82, v83
	v_cvt_pk_f16_f32 v82, v84, v85
	v_cvt_pk_f16_f32 v83, v86, v87
	s_add_u32 s76, s44, 0x10200
	s_addc_u32 s77, s45, 0
	global_store_dwordx4 v4, v[80:83], s[76:77] sc1
	s_waitcnt vmcnt(31)
	v_cvt_pk_f16_f32 v88, v88, v89
	v_cvt_pk_f16_f32 v89, v90, v91
	v_cvt_pk_f16_f32 v90, v92, v93
	v_cvt_pk_f16_f32 v91, v94, v95
	s_add_u32 s76, s44, 0x20200
	s_addc_u32 s77, s45, 0
	global_store_dwordx4 v4, v[88:91], s[76:77] sc1
	s_waitcnt vmcnt(30)
	v_cvt_pk_f16_f32 v96, v96, v97
	v_cvt_pk_f16_f32 v97, v98, v99
	v_cvt_pk_f16_f32 v98, v100, v101
	v_cvt_pk_f16_f32 v99, v102, v103
	s_add_u32 s76, s44, 0x30200
	s_addc_u32 s77, s45, 0
	global_store_dwordx4 v4, v[96:99], s[76:77] sc1
	s_waitcnt vmcnt(29)
	v_cvt_pk_f16_f32 v104, v104, v105
	v_cvt_pk_f16_f32 v105, v106, v107
	v_cvt_pk_f16_f32 v106, v108, v109
	v_cvt_pk_f16_f32 v107, v110, v111
	s_add_u32 s76, s46, 0x200
	s_addc_u32 s77, s47, 0
	global_store_dwordx4 v4, v[104:107], s[76:77] sc1
	s_waitcnt vmcnt(28)
	v_cvt_pk_f16_f32 v112, v112, v113
	v_cvt_pk_f16_f32 v113, v114, v115
	v_cvt_pk_f16_f32 v114, v116, v117
	v_cvt_pk_f16_f32 v115, v118, v119
	s_add_u32 s76, s46, 0x10200
	s_addc_u32 s77, s47, 0
	global_store_dwordx4 v4, v[112:115], s[76:77] sc1
	s_waitcnt vmcnt(27)
	v_cvt_pk_f16_f32 v120, v120, v121
	v_cvt_pk_f16_f32 v121, v122, v123
	v_cvt_pk_f16_f32 v122, v124, v125
	v_cvt_pk_f16_f32 v123, v126, v127
	s_add_u32 s76, s46, 0x20200
	s_addc_u32 s77, s47, 0
	global_store_dwordx4 v4, v[120:123], s[76:77] sc1
	s_waitcnt vmcnt(21)
	s_barrier
	s_mov_b64 s[56:57], exec
	s_and_b64 exec, exec, s[78:79]
	global_store_dword v6, v5, s[48:49] offset:0 sc1
	s_mov_b64 exec, s[56:57]
	s_add_u32 s58, s52, 0xc00
	s_addc_u32 s59, s53, 0
	global_load_dwordx4 v[72:75], v3, s[58:59] nt
	global_load_dwordx4 v[76:79], v3, s[58:59] offset:16 nt
	s_add_u32 s58, s52, 0x20c00
	s_addc_u32 s59, s53, 0
	global_load_dwordx4 v[80:83], v3, s[58:59] nt
	global_load_dwordx4 v[84:87], v3, s[58:59] offset:16 nt
	s_add_u32 s58, s52, 0x40c00
	s_addc_u32 s59, s53, 0
	global_load_dwordx4 v[88:91], v3, s[58:59] nt
	global_load_dwordx4 v[92:95], v3, s[58:59] offset:16 nt
	s_add_u32 s58, s52, 0x60c00
	s_addc_u32 s59, s53, 0
	global_load_dwordx4 v[96:99], v3, s[58:59] nt
	global_load_dwordx4 v[100:103], v3, s[58:59] offset:16 nt
	s_add_u32 s58, s54, 0xc00
	s_addc_u32 s59, s55, 0
	global_load_dwordx4 v[104:107], v3, s[58:59] nt
	global_load_dwordx4 v[108:111], v3, s[58:59] offset:16 nt
	s_add_u32 s58, s54, 0x20c00
	s_addc_u32 s59, s55, 0
	global_load_dwordx4 v[112:115], v3, s[58:59] nt
	global_load_dwordx4 v[116:119], v3, s[58:59] offset:16 nt
	s_add_u32 s58, s54, 0x40c00
	s_addc_u32 s59, s55, 0
	global_load_dwordx4 v[120:123], v3, s[58:59] nt
	global_load_dwordx4 v[124:127], v3, s[58:59] offset:16 nt
	s_waitcnt vmcnt(34)
	v_cvt_pk_f16_f32 v16, v16, v17
	v_cvt_pk_f16_f32 v17, v18, v19
	v_cvt_pk_f16_f32 v18, v20, v21
	v_cvt_pk_f16_f32 v19, v22, v23
	s_add_u32 s76, s44, 0x400
	s_addc_u32 s77, s45, 0
	global_store_dwordx4 v4, v[16:19], s[76:77] sc1
	s_waitcnt vmcnt(33)
	v_cvt_pk_f16_f32 v24, v24, v25
	v_cvt_pk_f16_f32 v25, v26, v27
	v_cvt_pk_f16_f32 v26, v28, v29
	v_cvt_pk_f16_f32 v27, v30, v31
	s_add_u32 s76, s44, 0x10400
	s_addc_u32 s77, s45, 0
	global_store_dwordx4 v4, v[24:27], s[76:77] sc1
	s_waitcnt vmcnt(32)
	v_cvt_pk_f16_f32 v32, v32, v33
	v_cvt_pk_f16_f32 v33, v34, v35
	v_cvt_pk_f16_f32 v34, v36, v37
	v_cvt_pk_f16_f32 v35, v38, v39
	s_add_u32 s76, s44, 0x20400
	s_addc_u32 s77, s45, 0
	global_store_dwordx4 v4, v[32:35], s[76:77] sc1
	s_waitcnt vmcnt(31)
	v_cvt_pk_f16_f32 v40, v40, v41
	v_cvt_pk_f16_f32 v41, v42, v43
	v_cvt_pk_f16_f32 v42, v44, v45
	v_cvt_pk_f16_f32 v43, v46, v47
	s_add_u32 s76, s44, 0x30400
	s_addc_u32 s77, s45, 0
	global_store_dwordx4 v4, v[40:43], s[76:77] sc1
	s_waitcnt vmcnt(30)
	v_cvt_pk_f16_f32 v48, v48, v49
	v_cvt_pk_f16_f32 v49, v50, v51
	v_cvt_pk_f16_f32 v50, v52, v53
	v_cvt_pk_f16_f32 v51, v54, v55
	s_add_u32 s76, s46, 0x400
	s_addc_u32 s77, s47, 0
	global_store_dwordx4 v4, v[48:51], s[76:77] sc1
	s_waitcnt vmcnt(29)
	v_cvt_pk_f16_f32 v56, v56, v57
	v_cvt_pk_f16_f32 v57, v58, v59
	v_cvt_pk_f16_f32 v58, v60, v61
	v_cvt_pk_f16_f32 v59, v62, v63
	s_add_u32 s76, s46, 0x10400
	s_addc_u32 s77, s47, 0
	global_store_dwordx4 v4, v[56:59], s[76:77] sc1
	s_waitcnt vmcnt(28)
	v_cvt_pk_f16_f32 v64, v64, v65
	v_cvt_pk_f16_f32 v65, v66, v67
	v_cvt_pk_f16_f32 v66, v68, v69
	v_cvt_pk_f16_f32 v67, v70, v71
	s_add_u32 s76, s46, 0x20400
	s_addc_u32 s77, s47, 0
	global_store_dwordx4 v4, v[64:67], s[76:77] sc1
	s_waitcnt vmcnt(22)
	s_barrier
	s_mov_b64 s[56:57], exec
	s_and_b64 exec, exec, s[78:79]
	global_store_dword v6, v5, s[48:49] offset:256 sc1
	s_mov_b64 exec, s[56:57]
	s_waitcnt vmcnt(20)
	v_cvt_pk_f16_f32 v72, v72, v73
	v_cvt_pk_f16_f32 v73, v74, v75
	v_cvt_pk_f16_f32 v74, v76, v77
	v_cvt_pk_f16_f32 v75, v78, v79
	s_add_u32 s76, s44, 0x600
	s_addc_u32 s77, s45, 0
	global_store_dwordx4 v4, v[72:75], s[76:77] sc1
	s_waitcnt vmcnt(19)
	v_cvt_pk_f16_f32 v80, v80, v81
	v_cvt_pk_f16_f32 v81, v82, v83
	v_cvt_pk_f16_f32 v82, v84, v85
	v_cvt_pk_f16_f32 v83, v86, v87
	s_add_u32 s76, s44, 0x10600
	s_addc_u32 s77, s45, 0
	global_store_dwordx4 v4, v[80:83], s[76:77] sc1
	s_waitcnt vmcnt(18)
	v_cvt_pk_f16_f32 v88, v88, v89
	v_cvt_pk_f16_f32 v89, v90, v91
	v_cvt_pk_f16_f32 v90, v92, v93
	v_cvt_pk_f16_f32 v91, v94, v95
	s_add_u32 s76, s44, 0x20600
	s_addc_u32 s77, s45, 0
	global_store_dwordx4 v4, v[88:91], s[76:77] sc1
	s_waitcnt vmcnt(17)
	v_cvt_pk_f16_f32 v96, v96, v97
	v_cvt_pk_f16_f32 v97, v98, v99
	v_cvt_pk_f16_f32 v98, v100, v101
	v_cvt_pk_f16_f32 v99, v102, v103
	s_add_u32 s76, s44, 0x30600
	s_addc_u32 s77, s45, 0
	global_store_dwordx4 v4, v[96:99], s[76:77] sc1
	s_waitcnt vmcnt(16)
	v_cvt_pk_f16_f32 v104, v104, v105
	v_cvt_pk_f16_f32 v105, v106, v107
	v_cvt_pk_f16_f32 v106, v108, v109
	v_cvt_pk_f16_f32 v107, v110, v111
	s_add_u32 s76, s46, 0x600
	s_addc_u32 s77, s47, 0
	global_store_dwordx4 v4, v[104:107], s[76:77] sc1
	s_waitcnt vmcnt(15)
	v_cvt_pk_f16_f32 v112, v112, v113
	v_cvt_pk_f16_f32 v113, v114, v115
	v_cvt_pk_f16_f32 v114, v116, v117
	v_cvt_pk_f16_f32 v115, v118, v119
	s_add_u32 s76, s46, 0x10600
	s_addc_u32 s77, s47, 0
	global_store_dwordx4 v4, v[112:115], s[76:77] sc1
	s_waitcnt vmcnt(14)
	v_cvt_pk_f16_f32 v120, v120, v121
	v_cvt_pk_f16_f32 v121, v122, v123
	v_cvt_pk_f16_f32 v122, v124, v125
	v_cvt_pk_f16_f32 v123, v126, v127
	s_add_u32 s76, s46, 0x20600
	s_addc_u32 s77, s47, 0
	global_store_dwordx4 v4, v[120:123], s[76:77] sc1
	s_waitcnt vmcnt(8)
	s_barrier
	s_mov_b64 s[56:57], exec
	s_and_b64 exec, exec, s[78:79]
	global_store_dword v6, v5, s[48:49] offset:512 sc1
	s_mov_b64 exec, s[56:57]
	s_waitcnt vmcnt(1)
	s_barrier
	s_mov_b64 s[56:57], exec
	s_and_b64 exec, exec, s[78:79]
	global_store_dword v6, v5, s[48:49] offset:768 sc1
	s_mov_b64 exec, s[56:57]
	s_add_i32 s24, s2, 0xffffff40
	s_lshl_b32 s20, s24, 4
	s_lshl_b32 s0, s24, 5
	s_ashr_i32 s21, s20, 31
	s_and_b32 s25, s0, 0xffffffc0
	s_lshl_b64 s[20:21], s[20:21], 2
	v_lshrrev_b32_e32 v6, 6, v0
	s_waitcnt lgkmcnt(0)
	s_add_u32 s26, s30, s20
	s_addc_u32 s27, s31, s21
	v_lshl_or_b32 v2, v6, 3, s25
	s_and_b32 s25, s2, 1
	s_lshl_b32 s2, s25, 7
	s_add_u32 s20, s28, s2
	v_and_b32_e32 v7, 63, v0
	s_mov_b32 s3, 0
	s_addc_u32 s21, s29, 0
	s_bfe_u32 s2, s24, 0x1a0001
	v_add_u32_e32 v2, v2, v7
	v_mov_b32_e32 v3, 0
	s_lshl_b64 s[2:3], s[2:3], 19
	v_lshl_add_u32 v1, v6, 2, 0
	v_lshlrev_b64 v[4:5], 8, v[2:3]
	v_lshl_or_b32 v2, v6, 16, s2
	s_lshl_b32 s2, s25, 12
	v_lshlrev_b32_e32 v6, 2, v7
	v_cmp_gt_u32_e64 s[0:1], 8, v7
	v_cmp_eq_u32_e64 s[22:23], 0, v7
	v_cmp_eq_u32_e64 s[6:7], 1, v7
	v_cmp_eq_u32_e64 s[8:9], 2, v7
	v_cmp_eq_u32_e64 s[10:11], 3, v7
	v_cmp_eq_u32_e64 s[12:13], 4, v7
	v_cmp_eq_u32_e64 s[14:15], 5, v7
	v_cmp_eq_u32_e64 s[16:17], 6, v7
	v_cmp_eq_u32_e64 s[18:19], 7, v7
	v_or3_b32 v6, v2, s2, v6
	v_mov_b32_e32 v7, s3
	v_cmp_eq_u32_e64 s[4:5], 0, v0
	v_lshl_add_u64 v[4:5], s[20:21], 0, v[4:5]
	v_lshl_add_u64 v[6:7], s[42:43], 0, v[6:7]
	s_mov_b64 s[28:29], 0
	s_lshr_b32 s58, s24, 1
	s_lshl_b32 s58, s58, 19
	s_add_u32 s60, s42, s58
	s_addc_u32 s61, s43, 0
	s_add_u32 s62, s60, 0x2000
	s_addc_u32 s63, s61, 0
	s_add_u32 s64, s62, 0x2000
	s_addc_u32 s65, s63, 0
	s_add_u32 s66, s64, 0x2000
	s_addc_u32 s67, s65, 0
	s_add_u32 s68, s66, 0x2000
	s_addc_u32 s69, s67, 0
	s_add_u32 s70, s68, 0x2000
	s_addc_u32 s71, s69, 0
	s_add_u32 s72, s70, 0x2000
	s_addc_u32 s73, s71, 0
	s_add_u32 s74, s72, 0x2000
	s_addc_u32 s75, s73, 0
	v_lshrrev_b32_e32 v96, 6, v0
	v_lshlrev_b32_e32 v96, 16, v96
	v_and_b32_e32 v97, 63, v0
	v_lshl_add_u32 v96, v97, 2, v96
	s_and_b32 s59, s24, 1
	s_lshl_b32 s59, s59, 12
	v_add_u32_e32 v96, s59, v96
	s_mov_b32 s76, 0
	s_mov_b32 s77, 0
	global_load_dword v100, v96, s[60:61] offset:0 nt
	global_load_dword v101, v96, s[62:63] offset:0 nt
	global_load_dword v102, v96, s[64:65] offset:0 nt
	global_load_dword v103, v96, s[66:67] offset:0 nt
	global_load_dword v104, v96, s[68:69] offset:0 nt
	global_load_dword v105, v96, s[70:71] offset:0 nt
	global_load_dword v106, v96, s[72:73] offset:0 nt
	global_load_dword v107, v96, s[74:75] offset:0 nt
	global_load_dword v108, v96, s[60:61] offset:256 nt
	global_load_dword v109, v96, s[62:63] offset:256 nt
	global_load_dword v110, v96, s[64:65] offset:256 nt
	global_load_dword v111, v96, s[66:67] offset:256 nt
	global_load_dword v112, v96, s[68:69] offset:256 nt
	global_load_dword v113, v96, s[70:71] offset:256 nt
	global_load_dword v114, v96, s[72:73] offset:256 nt
	global_load_dword v115, v96, s[74:75] offset:256 nt
	global_load_dword v116, v96, s[60:61] offset:512 nt
	global_load_dword v117, v96, s[62:63] offset:512 nt
	global_load_dword v118, v96, s[64:65] offset:512 nt
	global_load_dword v119, v96, s[66:67] offset:512 nt
	global_load_dword v120, v96, s[68:69] offset:512 nt
	global_load_dword v121, v96, s[70:71] offset:512 nt
	global_load_dword v122, v96, s[72:73] offset:512 nt
	global_load_dword v123, v96, s[74:75] offset:512 nt
	global_load_dword v124, v96, s[60:61] offset:768 nt
	global_load_dword v125, v96, s[62:63] offset:768 nt
	global_load_dword v126, v96, s[64:65] offset:768 nt
	global_load_dword v127, v96, s[66:67] offset:768 nt
	global_load_dword v128, v96, s[68:69] offset:768 nt
	global_load_dword v129, v96, s[70:71] offset:768 nt
	global_load_dword v130, v96, s[72:73] offset:768 nt
	global_load_dword v131, v96, s[74:75] offset:768 nt
	global_load_dword v132, v96, s[60:61] offset:1024 nt
	global_load_dword v133, v96, s[62:63] offset:1024 nt
	global_load_dword v134, v96, s[64:65] offset:1024 nt
	global_load_dword v135, v96, s[66:67] offset:1024 nt
	global_load_dword v136, v96, s[68:69] offset:1024 nt
	global_load_dword v137, v96, s[70:71] offset:1024 nt
	global_load_dword v138, v96, s[72:73] offset:1024 nt
	global_load_dword v139, v96, s[74:75] offset:1024 nt
	global_load_dword v140, v96, s[60:61] offset:1280 nt
	global_load_dword v141, v96, s[62:63] offset:1280 nt
	global_load_dword v142, v96, s[64:65] offset:1280 nt
	global_load_dword v143, v96, s[66:67] offset:1280 nt
	global_load_dword v144, v96, s[68:69] offset:1280 nt
	global_load_dword v145, v96, s[70:71] offset:1280 nt
	global_load_dword v146, v96, s[72:73] offset:1280 nt
	global_load_dword v147, v96, s[74:75] offset:1280 nt
	global_load_dword v148, v96, s[60:61] offset:1536 nt
	global_load_dword v149, v96, s[62:63] offset:1536 nt
	global_load_dword v150, v96, s[64:65] offset:1536 nt
	global_load_dword v151, v96, s[66:67] offset:1536 nt
	global_load_dword v152, v96, s[68:69] offset:1536 nt
	global_load_dword v153, v96, s[70:71] offset:1536 nt
	global_load_dword v154, v96, s[72:73] offset:1536 nt
	global_load_dword v155, v96, s[74:75] offset:1536 nt
	s_waitcnt vmcnt(48)
	v_cmp_ne_u32_e32 vcc, 0, v100
	s_nop 1
	v_mov_b32_e32 v2, vcc_lo
	v_mov_b32_e32 v9, vcc_hi
	v_cmp_ne_u32_e32 vcc, 0, v101
	v_cndmask_b32_e64 v2, 0, v2, s[22:23]
	v_cndmask_b32_e64 v9, 0, v9, s[22:23]
	v_mov_b32_e32 v11, vcc_hi
	v_mov_b32_e32 v14, vcc_lo
	v_cndmask_b32_e64 v9, v9, v11, s[6:7]
	v_cndmask_b32_e64 v2, v2, v14, s[6:7]
	v_cmp_ne_u32_e32 vcc, 0, v102
	s_nop 1
	v_mov_b32_e32 v11, vcc_lo
	v_mov_b32_e32 v14, vcc_hi
	v_cmp_ne_u32_e32 vcc, 0, v103
	v_cndmask_b32_e64 v2, v2, v11, s[8:9]
	v_cndmask_b32_e64 v9, v9, v14, s[8:9]
	v_mov_b32_e32 v11, vcc_hi
	v_mov_b32_e32 v14, vcc_lo
	v_cmp_ne_u32_e32 vcc, 0, v104
	v_cndmask_b32_e64 v9, v9, v11, s[10:11]
	v_cndmask_b32_e64 v2, v2, v14, s[10:11]
	v_mov_b32_e32 v11, vcc_lo
	v_mov_b32_e32 v12, vcc_hi
	v_cmp_ne_u32_e32 vcc, 0, v105
	v_cndmask_b32_e64 v2, v2, v11, s[12:13]
	v_cndmask_b32_e64 v9, v9, v12, s[12:13]
	v_mov_b32_e32 v11, vcc_hi
	v_mov_b32_e32 v12, vcc_lo
	v_cndmask_b32_e64 v9, v9, v11, s[14:15]
	v_cndmask_b32_e64 v2, v2, v12, s[14:15]
	v_cmp_ne_u32_e32 vcc, 0, v106
	s_nop 1
	v_mov_b32_e32 v10, vcc_lo
	v_mov_b32_e32 v11, vcc_hi
	v_cmp_ne_u32_e32 vcc, 0, v107
	v_cndmask_b32_e64 v2, v2, v10, s[16:17]
	v_cndmask_b32_e64 v8, v9, v11, s[16:17]
	v_mov_b32_e32 v9, vcc_hi
	v_mov_b32_e32 v10, vcc_lo
	v_cndmask_b32_e64 v9, v8, v9, s[18:19]
	v_cndmask_b32_e64 v8, v2, v10, s[18:19]
	s_mov_b64 s[2:3], exec
	s_mov_b64 exec, s[0:1]
	global_store_dwordx2 v[4:5], v[8:9], off
	s_mov_b64 exec, s[2:3]
	v_cmp_ne_u64_e32 vcc, 0, v[8:9]
	s_and_b64 s[20:21], s[0:1], vcc
	s_cmp_lg_u64 s[20:21], 0
	s_cselect_b32 s20, 1, 0
	s_or_b32 s76, s76, s20
	v_cmp_ne_u64_e32 vcc, -1, v[8:9]
	s_and_b64 s[20:21], s[0:1], vcc
	s_cmp_lg_u64 s[20:21], 0
	s_cselect_b32 s20, 1, 0
	s_or_b32 s77, s77, s20
	v_lshl_add_u64 v[4:5], v[4:5], 0, 8
	global_load_dword v156, v96, s[60:61] offset:1792 nt
	global_load_dword v157, v96, s[62:63] offset:1792 nt
	global_load_dword v158, v96, s[64:65] offset:1792 nt
	global_load_dword v159, v96, s[66:67] offset:1792 nt
	global_load_dword v160, v96, s[68:69] offset:1792 nt
	global_load_dword v161, v96, s[70:71] offset:1792 nt
	global_load_dword v162, v96, s[72:73] offset:1792 nt
	global_load_dword v163, v96, s[74:75] offset:1792 nt
	s_waitcnt vmcnt(49)
	v_cmp_ne_u32_e32 vcc, 0, v108
	s_nop 1
	v_mov_b32_e32 v2, vcc_lo
	v_mov_b32_e32 v9, vcc_hi
	v_cmp_ne_u32_e32 vcc, 0, v109
	v_cndmask_b32_e64 v2, 0, v2, s[22:23]
	v_cndmask_b32_e64 v9, 0, v9, s[22:23]
	v_mov_b32_e32 v11, vcc_hi
	v_mov_b32_e32 v14, vcc_lo
	v_cndmask_b32_e64 v9, v9, v11, s[6:7]
	v_cndmask_b32_e64 v2, v2, v14, s[6:7]
	v_cmp_ne_u32_e32 vcc, 0, v110
	s_nop 1
	v_mov_b32_e32 v11, vcc_lo
	v_mov_b32_e32 v14, vcc_hi
	v_cmp_ne_u32_e32 vcc, 0, v111
	v_cndmask_b32_e64 v2, v2, v11, s[8:9]
	v_cndmask_b32_e64 v9, v9, v14, s[8:9]
	v_mov_b32_e32 v11, vcc_hi
	v_mov_b32_e32 v14, vcc_lo
	v_cmp_ne_u32_e32 vcc, 0, v112
	v_cndmask_b32_e64 v9, v9, v11, s[10:11]
	v_cndmask_b32_e64 v2, v2, v14, s[10:11]
	v_mov_b32_e32 v11, vcc_lo
	v_mov_b32_e32 v12, vcc_hi
	v_cmp_ne_u32_e32 vcc, 0, v113
	v_cndmask_b32_e64 v2, v2, v11, s[12:13]
	v_cndmask_b32_e64 v9, v9, v12, s[12:13]
	v_mov_b32_e32 v11, vcc_hi
	v_mov_b32_e32 v12, vcc_lo
	v_cndmask_b32_e64 v9, v9, v11, s[14:15]
	v_cndmask_b32_e64 v2, v2, v12, s[14:15]
	v_cmp_ne_u32_e32 vcc, 0, v114
	s_nop 1
	v_mov_b32_e32 v10, vcc_lo
	v_mov_b32_e32 v11, vcc_hi
	v_cmp_ne_u32_e32 vcc, 0, v115
	v_cndmask_b32_e64 v2, v2, v10, s[16:17]
	v_cndmask_b32_e64 v8, v9, v11, s[16:17]
	v_mov_b32_e32 v9, vcc_hi
	v_mov_b32_e32 v10, vcc_lo
	v_cndmask_b32_e64 v9, v8, v9, s[18:19]
	v_cndmask_b32_e64 v8, v2, v10, s[18:19]
	s_mov_b64 s[2:3], exec
	s_mov_b64 exec, s[0:1]
	global_store_dwordx2 v[4:5], v[8:9], off
	s_mov_b64 exec, s[2:3]
	v_cmp_ne_u64_e32 vcc, 0, v[8:9]
	s_and_b64 s[20:21], s[0:1], vcc
	s_cmp_lg_u64 s[20:21], 0
	s_cselect_b32 s20, 2, 0
	s_or_b32 s76, s76, s20
	v_cmp_ne_u64_e32 vcc, -1, v[8:9]
	s_and_b64 s[20:21], s[0:1], vcc
	s_cmp_lg_u64 s[20:21], 0
	s_cselect_b32 s20, 2, 0
	s_or_b32 s77, s77, s20
	v_lshl_add_u64 v[4:5], v[4:5], 0, 8
	global_load_dword v164, v96, s[60:61] offset:2048 nt
	global_load_dword v165, v96, s[62:63] offset:2048 nt
	global_load_dword v166, v96, s[64:65] offset:2048 nt
	global_load_dword v167, v96, s[66:67] offset:2048 nt
	global_load_dword v168, v96, s[68:69] offset:2048 nt
	global_load_dword v169, v96, s[70:71] offset:2048 nt
	global_load_dword v170, v96, s[72:73] offset:2048 nt
	global_load_dword v171, v96, s[74:75] offset:2048 nt
	s_waitcnt vmcnt(50)
	v_cmp_ne_u32_e32 vcc, 0, v116
	s_nop 1
	v_mov_b32_e32 v2, vcc_lo
	v_mov_b32_e32 v9, vcc_hi
	v_cmp_ne_u32_e32 vcc, 0, v117
	v_cndmask_b32_e64 v2, 0, v2, s[22:23]
	v_cndmask_b32_e64 v9, 0, v9, s[22:23]
	v_mov_b32_e32 v11, vcc_hi
	v_mov_b32_e32 v14, vcc_lo
	v_cndmask_b32_e64 v9, v9, v11, s[6:7]
	v_cndmask_b32_e64 v2, v2, v14, s[6:7]
	v_cmp_ne_u32_e32 vcc, 0, v118
	s_nop 1
	v_mov_b32_e32 v11, vcc_lo
	v_mov_b32_e32 v14, vcc_hi
	v_cmp_ne_u32_e32 vcc, 0, v119
	v_cndmask_b32_e64 v2, v2, v11, s[8:9]
	v_cndmask_b32_e64 v9, v9, v14, s[8:9]
	v_mov_b32_e32 v11, vcc_hi
	v_mov_b32_e32 v14, vcc_lo
	v_cmp_ne_u32_e32 vcc, 0, v120
	v_cndmask_b32_e64 v9, v9, v11, s[10:11]
	v_cndmask_b32_e64 v2, v2, v14, s[10:11]
	v_mov_b32_e32 v11, vcc_lo
	v_mov_b32_e32 v12, vcc_hi
	v_cmp_ne_u32_e32 vcc, 0, v121
	v_cndmask_b32_e64 v2, v2, v11, s[12:13]
	v_cndmask_b32_e64 v9, v9, v12, s[12:13]
	v_mov_b32_e32 v11, vcc_hi
	v_mov_b32_e32 v12, vcc_lo
	v_cndmask_b32_e64 v9, v9, v11, s[14:15]
	v_cndmask_b32_e64 v2, v2, v12, s[14:15]
	v_cmp_ne_u32_e32 vcc, 0, v122
	s_nop 1
	v_mov_b32_e32 v10, vcc_lo
	v_mov_b32_e32 v11, vcc_hi
	v_cmp_ne_u32_e32 vcc, 0, v123
	v_cndmask_b32_e64 v2, v2, v10, s[16:17]
	v_cndmask_b32_e64 v8, v9, v11, s[16:17]
	v_mov_b32_e32 v9, vcc_hi
	v_mov_b32_e32 v10, vcc_lo
	v_cndmask_b32_e64 v9, v8, v9, s[18:19]
	v_cndmask_b32_e64 v8, v2, v10, s[18:19]
	s_mov_b64 s[2:3], exec
	s_mov_b64 exec, s[0:1]
	global_store_dwordx2 v[4:5], v[8:9], off
	s_mov_b64 exec, s[2:3]
	v_cmp_ne_u64_e32 vcc, 0, v[8:9]
	s_and_b64 s[20:21], s[0:1], vcc
	s_cmp_lg_u64 s[20:21], 0
	s_cselect_b32 s20, 4, 0
	s_or_b32 s76, s76, s20
	v_cmp_ne_u64_e32 vcc, -1, v[8:9]
	s_and_b64 s[20:21], s[0:1], vcc
	s_cmp_lg_u64 s[20:21], 0
	s_cselect_b32 s20, 4, 0
	s_or_b32 s77, s77, s20
	v_lshl_add_u64 v[4:5], v[4:5], 0, 8
	global_load_dword v172, v96, s[60:61] offset:2304 nt
	global_load_dword v173, v96, s[62:63] offset:2304 nt
	global_load_dword v174, v96, s[64:65] offset:2304 nt
	global_load_dword v175, v96, s[66:67] offset:2304 nt
	global_load_dword v176, v96, s[68:69] offset:2304 nt
	global_load_dword v177, v96, s[70:71] offset:2304 nt
	global_load_dword v178, v96, s[72:73] offset:2304 nt
	global_load_dword v179, v96, s[74:75] offset:2304 nt
	s_waitcnt vmcnt(51)
	v_cmp_ne_u32_e32 vcc, 0, v124
	s_nop 1
	v_mov_b32_e32 v2, vcc_lo
	v_mov_b32_e32 v9, vcc_hi
	v_cmp_ne_u32_e32 vcc, 0, v125
	v_cndmask_b32_e64 v2, 0, v2, s[22:23]
	v_cndmask_b32_e64 v9, 0, v9, s[22:23]
	v_mov_b32_e32 v11, vcc_hi
	v_mov_b32_e32 v14, vcc_lo
	v_cndmask_b32_e64 v9, v9, v11, s[6:7]
	v_cndmask_b32_e64 v2, v2, v14, s[6:7]
	v_cmp_ne_u32_e32 vcc, 0, v126
	s_nop 1
	v_mov_b32_e32 v11, vcc_lo
	v_mov_b32_e32 v14, vcc_hi
	v_cmp_ne_u32_e32 vcc, 0, v127
	v_cndmask_b32_e64 v2, v2, v11, s[8:9]
	v_cndmask_b32_e64 v9, v9, v14, s[8:9]
	v_mov_b32_e32 v11, vcc_hi
	v_mov_b32_e32 v14, vcc_lo
	v_cmp_ne_u32_e32 vcc, 0, v128
	v_cndmask_b32_e64 v9, v9, v11, s[10:11]
	v_cndmask_b32_e64 v2, v2, v14, s[10:11]
	v_mov_b32_e32 v11, vcc_lo
	v_mov_b32_e32 v12, vcc_hi
	v_cmp_ne_u32_e32 vcc, 0, v129
	v_cndmask_b32_e64 v2, v2, v11, s[12:13]
	v_cndmask_b32_e64 v9, v9, v12, s[12:13]
	v_mov_b32_e32 v11, vcc_hi
	v_mov_b32_e32 v12, vcc_lo
	v_cndmask_b32_e64 v9, v9, v11, s[14:15]
	v_cndmask_b32_e64 v2, v2, v12, s[14:15]
	v_cmp_ne_u32_e32 vcc, 0, v130
	s_nop 1
	v_mov_b32_e32 v10, vcc_lo
	v_mov_b32_e32 v11, vcc_hi
	v_cmp_ne_u32_e32 vcc, 0, v131
	v_cndmask_b32_e64 v2, v2, v10, s[16:17]
	v_cndmask_b32_e64 v8, v9, v11, s[16:17]
	v_mov_b32_e32 v9, vcc_hi
	v_mov_b32_e32 v10, vcc_lo
	v_cndmask_b32_e64 v9, v8, v9, s[18:19]
	v_cndmask_b32_e64 v8, v2, v10, s[18:19]
	s_mov_b64 s[2:3], exec
	s_mov_b64 exec, s[0:1]
	global_store_dwordx2 v[4:5], v[8:9], off
	s_mov_b64 exec, s[2:3]
	v_cmp_ne_u64_e32 vcc, 0, v[8:9]
	s_and_b64 s[20:21], s[0:1], vcc
	s_cmp_lg_u64 s[20:21], 0
	s_cselect_b32 s20, 8, 0
	s_or_b32 s76, s76, s20
	v_cmp_ne_u64_e32 vcc, -1, v[8:9]
	s_and_b64 s[20:21], s[0:1], vcc
	s_cmp_lg_u64 s[20:21], 0
	s_cselect_b32 s20, 8, 0
	s_or_b32 s77, s77, s20
	v_lshl_add_u64 v[4:5], v[4:5], 0, 8
	global_load_dword v180, v96, s[60:61] offset:2560 nt
	global_load_dword v181, v96, s[62:63] offset:2560 nt
	global_load_dword v182, v96, s[64:65] offset:2560 nt
	global_load_dword v183, v96, s[66:67] offset:2560 nt
	global_load_dword v184, v96, s[68:69] offset:2560 nt
	global_load_dword v185, v96, s[70:71] offset:2560 nt
	global_load_dword v186, v96, s[72:73] offset:2560 nt
	global_load_dword v187, v96, s[74:75] offset:2560 nt
	s_waitcnt vmcnt(52)
	v_cmp_ne_u32_e32 vcc, 0, v132
	s_nop 1
	v_mov_b32_e32 v2, vcc_lo
	v_mov_b32_e32 v9, vcc_hi
	v_cmp_ne_u32_e32 vcc, 0, v133
	v_cndmask_b32_e64 v2, 0, v2, s[22:23]
	v_cndmask_b32_e64 v9, 0, v9, s[22:23]
	v_mov_b32_e32 v11, vcc_hi
	v_mov_b32_e32 v14, vcc_lo
	v_cndmask_b32_e64 v9, v9, v11, s[6:7]
	v_cndmask_b32_e64 v2, v2, v14, s[6:7]
	v_cmp_ne_u32_e32 vcc, 0, v134
	s_nop 1
	v_mov_b32_e32 v11, vcc_lo
	v_mov_b32_e32 v14, vcc_hi
	v_cmp_ne_u32_e32 vcc, 0, v135
	v_cndmask_b32_e64 v2, v2, v11, s[8:9]
	v_cndmask_b32_e64 v9, v9, v14, s[8:9]
	v_mov_b32_e32 v11, vcc_hi
	v_mov_b32_e32 v14, vcc_lo
	v_cmp_ne_u32_e32 vcc, 0, v136
	v_cndmask_b32_e64 v9, v9, v11, s[10:11]
	v_cndmask_b32_e64 v2, v2, v14, s[10:11]
	v_mov_b32_e32 v11, vcc_lo
	v_mov_b32_e32 v12, vcc_hi
	v_cmp_ne_u32_e32 vcc, 0, v137
	v_cndmask_b32_e64 v2, v2, v11, s[12:13]
	v_cndmask_b32_e64 v9, v9, v12, s[12:13]
	v_mov_b32_e32 v11, vcc_hi
	v_mov_b32_e32 v12, vcc_lo
	v_cndmask_b32_e64 v9, v9, v11, s[14:15]
	v_cndmask_b32_e64 v2, v2, v12, s[14:15]
	v_cmp_ne_u32_e32 vcc, 0, v138
	s_nop 1
	v_mov_b32_e32 v10, vcc_lo
	v_mov_b32_e32 v11, vcc_hi
	v_cmp_ne_u32_e32 vcc, 0, v139
	v_cndmask_b32_e64 v2, v2, v10, s[16:17]
	v_cndmask_b32_e64 v8, v9, v11, s[16:17]
	v_mov_b32_e32 v9, vcc_hi
	v_mov_b32_e32 v10, vcc_lo
	v_cndmask_b32_e64 v9, v8, v9, s[18:19]
	v_cndmask_b32_e64 v8, v2, v10, s[18:19]
	s_mov_b64 s[2:3], exec
	s_mov_b64 exec, s[0:1]
	global_store_dwordx2 v[4:5], v[8:9], off
	s_mov_b64 exec, s[2:3]
	v_cmp_ne_u64_e32 vcc, 0, v[8:9]
	s_and_b64 s[20:21], s[0:1], vcc
	s_cmp_lg_u64 s[20:21], 0
	s_cselect_b32 s20, 16, 0
	s_or_b32 s76, s76, s20
	v_cmp_ne_u64_e32 vcc, -1, v[8:9]
	s_and_b64 s[20:21], s[0:1], vcc
	s_cmp_lg_u64 s[20:21], 0
	s_cselect_b32 s20, 16, 0
	s_or_b32 s77, s77, s20
	v_lshl_add_u64 v[4:5], v[4:5], 0, 8
	global_load_dword v188, v96, s[60:61] offset:2816 nt
	global_load_dword v189, v96, s[62:63] offset:2816 nt
	global_load_dword v190, v96, s[64:65] offset:2816 nt
	global_load_dword v191, v96, s[66:67] offset:2816 nt
	global_load_dword v192, v96, s[68:69] offset:2816 nt
	global_load_dword v193, v96, s[70:71] offset:2816 nt
	global_load_dword v194, v96, s[72:73] offset:2816 nt
	global_load_dword v195, v96, s[74:75] offset:2816 nt
	s_waitcnt vmcnt(53)
	v_cmp_ne_u32_e32 vcc, 0, v140
	s_nop 1
	v_mov_b32_e32 v2, vcc_lo
	v_mov_b32_e32 v9, vcc_hi
	v_cmp_ne_u32_e32 vcc, 0, v141
	v_cndmask_b32_e64 v2, 0, v2, s[22:23]
	v_cndmask_b32_e64 v9, 0, v9, s[22:23]
	v_mov_b32_e32 v11, vcc_hi
	v_mov_b32_e32 v14, vcc_lo
	v_cndmask_b32_e64 v9, v9, v11, s[6:7]
	v_cndmask_b32_e64 v2, v2, v14, s[6:7]
	v_cmp_ne_u32_e32 vcc, 0, v142
	s_nop 1
	v_mov_b32_e32 v11, vcc_lo
	v_mov_b32_e32 v14, vcc_hi
	v_cmp_ne_u32_e32 vcc, 0, v143
	v_cndmask_b32_e64 v2, v2, v11, s[8:9]
	v_cndmask_b32_e64 v9, v9, v14, s[8:9]
	v_mov_b32_e32 v11, vcc_hi
	v_mov_b32_e32 v14, vcc_lo
	v_cmp_ne_u32_e32 vcc, 0, v144
	v_cndmask_b32_e64 v9, v9, v11, s[10:11]
	v_cndmask_b32_e64 v2, v2, v14, s[10:11]
	v_mov_b32_e32 v11, vcc_lo
	v_mov_b32_e32 v12, vcc_hi
	v_cmp_ne_u32_e32 vcc, 0, v145
	v_cndmask_b32_e64 v2, v2, v11, s[12:13]
	v_cndmask_b32_e64 v9, v9, v12, s[12:13]
	v_mov_b32_e32 v11, vcc_hi
	v_mov_b32_e32 v12, vcc_lo
	v_cndmask_b32_e64 v9, v9, v11, s[14:15]
	v_cndmask_b32_e64 v2, v2, v12, s[14:15]
	v_cmp_ne_u32_e32 vcc, 0, v146
	s_nop 1
	v_mov_b32_e32 v10, vcc_lo
	v_mov_b32_e32 v11, vcc_hi
	v_cmp_ne_u32_e32 vcc, 0, v147
	v_cndmask_b32_e64 v2, v2, v10, s[16:17]
	v_cndmask_b32_e64 v8, v9, v11, s[16:17]
	v_mov_b32_e32 v9, vcc_hi
	v_mov_b32_e32 v10, vcc_lo
	v_cndmask_b32_e64 v9, v8, v9, s[18:19]
	v_cndmask_b32_e64 v8, v2, v10, s[18:19]
	s_mov_b64 s[2:3], exec
	s_mov_b64 exec, s[0:1]
	global_store_dwordx2 v[4:5], v[8:9], off
	s_mov_b64 exec, s[2:3]
	v_cmp_ne_u64_e32 vcc, 0, v[8:9]
	s_and_b64 s[20:21], s[0:1], vcc
	s_cmp_lg_u64 s[20:21], 0
	s_cselect_b32 s20, 32, 0
	s_or_b32 s76, s76, s20
	v_cmp_ne_u64_e32 vcc, -1, v[8:9]
	s_and_b64 s[20:21], s[0:1], vcc
	s_cmp_lg_u64 s[20:21], 0
	s_cselect_b32 s20, 32, 0
	s_or_b32 s77, s77, s20
	v_lshl_add_u64 v[4:5], v[4:5], 0, 8
	global_load_dword v196, v96, s[60:61] offset:3072 nt
	global_load_dword v197, v96, s[62:63] offset:3072 nt
	global_load_dword v198, v96, s[64:65] offset:3072 nt
	global_load_dword v199, v96, s[66:67] offset:3072 nt
	global_load_dword v200, v96, s[68:69] offset:3072 nt
	global_load_dword v201, v96, s[70:71] offset:3072 nt
	global_load_dword v202, v96, s[72:73] offset:3072 nt
	global_load_dword v203, v96, s[74:75] offset:3072 nt
	s_waitcnt vmcnt(54)
	v_cmp_ne_u32_e32 vcc, 0, v148
	s_nop 1
	v_mov_b32_e32 v2, vcc_lo
	v_mov_b32_e32 v9, vcc_hi
	v_cmp_ne_u32_e32 vcc, 0, v149
	v_cndmask_b32_e64 v2, 0, v2, s[22:23]
	v_cndmask_b32_e64 v9, 0, v9, s[22:23]
	v_mov_b32_e32 v11, vcc_hi
	v_mov_b32_e32 v14, vcc_lo
	v_cndmask_b32_e64 v9, v9, v11, s[6:7]
	v_cndmask_b32_e64 v2, v2, v14, s[6:7]
	v_cmp_ne_u32_e32 vcc, 0, v150
	s_nop 1
	v_mov_b32_e32 v11, vcc_lo
	v_mov_b32_e32 v14, vcc_hi
	v_cmp_ne_u32_e32 vcc, 0, v151
	v_cndmask_b32_e64 v2, v2, v11, s[8:9]
	v_cndmask_b32_e64 v9, v9, v14, s[8:9]
	v_mov_b32_e32 v11, vcc_hi
	v_mov_b32_e32 v14, vcc_lo
	v_cmp_ne_u32_e32 vcc, 0, v152
	v_cndmask_b32_e64 v9, v9, v11, s[10:11]
	v_cndmask_b32_e64 v2, v2, v14, s[10:11]
	v_mov_b32_e32 v11, vcc_lo
	v_mov_b32_e32 v12, vcc_hi
	v_cmp_ne_u32_e32 vcc, 0, v153
	v_cndmask_b32_e64 v2, v2, v11, s[12:13]
	v_cndmask_b32_e64 v9, v9, v12, s[12:13]
	v_mov_b32_e32 v11, vcc_hi
	v_mov_b32_e32 v12, vcc_lo
	v_cndmask_b32_e64 v9, v9, v11, s[14:15]
	v_cndmask_b32_e64 v2, v2, v12, s[14:15]
	v_cmp_ne_u32_e32 vcc, 0, v154
	s_nop 1
	v_mov_b32_e32 v10, vcc_lo
	v_mov_b32_e32 v11, vcc_hi
	v_cmp_ne_u32_e32 vcc, 0, v155
	v_cndmask_b32_e64 v2, v2, v10, s[16:17]
	v_cndmask_b32_e64 v8, v9, v11, s[16:17]
	v_mov_b32_e32 v9, vcc_hi
	v_mov_b32_e32 v10, vcc_lo
	v_cndmask_b32_e64 v9, v8, v9, s[18:19]
	v_cndmask_b32_e64 v8, v2, v10, s[18:19]
	s_mov_b64 s[2:3], exec
	s_mov_b64 exec, s[0:1]
	global_store_dwordx2 v[4:5], v[8:9], off
	s_mov_b64 exec, s[2:3]
	v_cmp_ne_u64_e32 vcc, 0, v[8:9]
	s_and_b64 s[20:21], s[0:1], vcc
	s_cmp_lg_u64 s[20:21], 0
	s_cselect_b32 s20, 64, 0
	s_or_b32 s76, s76, s20
	v_cmp_ne_u64_e32 vcc, -1, v[8:9]
	s_and_b64 s[20:21], s[0:1], vcc
	s_cmp_lg_u64 s[20:21], 0
	s_cselect_b32 s20, 64, 0
	s_or_b32 s77, s77, s20
	v_lshl_add_u64 v[4:5], v[4:5], 0, 8
	global_load_dword v204, v96, s[60:61] offset:3328 nt
	global_load_dword v205, v96, s[62:63] offset:3328 nt
	global_load_dword v206, v96, s[64:65] offset:3328 nt
	global_load_dword v207, v96, s[66:67] offset:3328 nt
	global_load_dword v208, v96, s[68:69] offset:3328 nt
	global_load_dword v209, v96, s[70:71] offset:3328 nt
	global_load_dword v210, v96, s[72:73] offset:3328 nt
	global_load_dword v211, v96, s[74:75] offset:3328 nt
	s_waitcnt vmcnt(54)
	v_cmp_ne_u32_e32 vcc, 0, v156
	s_nop 1
	v_mov_b32_e32 v2, vcc_lo
	v_mov_b32_e32 v9, vcc_hi
	v_cmp_ne_u32_e32 vcc, 0, v157
	v_cndmask_b32_e64 v2, 0, v2, s[22:23]
	v_cndmask_b32_e64 v9, 0, v9, s[22:23]
	v_mov_b32_e32 v11, vcc_hi
	v_mov_b32_e32 v14, vcc_lo
	v_cndmask_b32_e64 v9, v9, v11, s[6:7]
	v_cndmask_b32_e64 v2, v2, v14, s[6:7]
	v_cmp_ne_u32_e32 vcc, 0, v158
	s_nop 1
	v_mov_b32_e32 v11, vcc_lo
	v_mov_b32_e32 v14, vcc_hi
	v_cmp_ne_u32_e32 vcc, 0, v159
	v_cndmask_b32_e64 v2, v2, v11, s[8:9]
	v_cndmask_b32_e64 v9, v9, v14, s[8:9]
	v_mov_b32_e32 v11, vcc_hi
	v_mov_b32_e32 v14, vcc_lo
	v_cmp_ne_u32_e32 vcc, 0, v160
	v_cndmask_b32_e64 v9, v9, v11, s[10:11]
	v_cndmask_b32_e64 v2, v2, v14, s[10:11]
	v_mov_b32_e32 v11, vcc_lo
	v_mov_b32_e32 v12, vcc_hi
	v_cmp_ne_u32_e32 vcc, 0, v161
	v_cndmask_b32_e64 v2, v2, v11, s[12:13]
	v_cndmask_b32_e64 v9, v9, v12, s[12:13]
	v_mov_b32_e32 v11, vcc_hi
	v_mov_b32_e32 v12, vcc_lo
	v_cndmask_b32_e64 v9, v9, v11, s[14:15]
	v_cndmask_b32_e64 v2, v2, v12, s[14:15]
	v_cmp_ne_u32_e32 vcc, 0, v162
	s_nop 1
	v_mov_b32_e32 v10, vcc_lo
	v_mov_b32_e32 v11, vcc_hi
	v_cmp_ne_u32_e32 vcc, 0, v163
	v_cndmask_b32_e64 v2, v2, v10, s[16:17]
	v_cndmask_b32_e64 v8, v9, v11, s[16:17]
	v_mov_b32_e32 v9, vcc_hi
	v_mov_b32_e32 v10, vcc_lo
	v_cndmask_b32_e64 v9, v8, v9, s[18:19]
	v_cndmask_b32_e64 v8, v2, v10, s[18:19]
	s_mov_b64 s[2:3], exec
	s_mov_b64 exec, s[0:1]
	global_store_dwordx2 v[4:5], v[8:9], off
	s_mov_b64 exec, s[2:3]
	v_cmp_ne_u64_e32 vcc, 0, v[8:9]
	s_and_b64 s[20:21], s[0:1], vcc
	s_cmp_lg_u64 s[20:21], 0
	s_cselect_b32 s20, 128, 0
	s_or_b32 s76, s76, s20
	v_cmp_ne_u64_e32 vcc, -1, v[8:9]
	s_and_b64 s[20:21], s[0:1], vcc
	s_cmp_lg_u64 s[20:21], 0
	s_cselect_b32 s20, 128, 0
	s_or_b32 s77, s77, s20
	v_lshl_add_u64 v[4:5], v[4:5], 0, 8
	global_load_dword v212, v96, s[60:61] offset:3584 nt
	global_load_dword v213, v96, s[62:63] offset:3584 nt
	global_load_dword v214, v96, s[64:65] offset:3584 nt
	global_load_dword v215, v96, s[66:67] offset:3584 nt
	global_load_dword v216, v96, s[68:69] offset:3584 nt
	global_load_dword v217, v96, s[70:71] offset:3584 nt
	global_load_dword v218, v96, s[72:73] offset:3584 nt
	global_load_dword v219, v96, s[74:75] offset:3584 nt
	s_waitcnt vmcnt(54)
	v_cmp_ne_u32_e32 vcc, 0, v164
	s_nop 1
	v_mov_b32_e32 v2, vcc_lo
	v_mov_b32_e32 v9, vcc_hi
	v_cmp_ne_u32_e32 vcc, 0, v165
	v_cndmask_b32_e64 v2, 0, v2, s[22:23]
	v_cndmask_b32_e64 v9, 0, v9, s[22:23]
	v_mov_b32_e32 v11, vcc_hi
	v_mov_b32_e32 v14, vcc_lo
	v_cndmask_b32_e64 v9, v9, v11, s[6:7]
	v_cndmask_b32_e64 v2, v2, v14, s[6:7]
	v_cmp_ne_u32_e32 vcc, 0, v166
	s_nop 1
	v_mov_b32_e32 v11, vcc_lo
	v_mov_b32_e32 v14, vcc_hi
	v_cmp_ne_u32_e32 vcc, 0, v167
	v_cndmask_b32_e64 v2, v2, v11, s[8:9]
	v_cndmask_b32_e64 v9, v9, v14, s[8:9]
	v_mov_b32_e32 v11, vcc_hi
	v_mov_b32_e32 v14, vcc_lo
	v_cmp_ne_u32_e32 vcc, 0, v168
	v_cndmask_b32_e64 v9, v9, v11, s[10:11]
	v_cndmask_b32_e64 v2, v2, v14, s[10:11]
	v_mov_b32_e32 v11, vcc_lo
	v_mov_b32_e32 v12, vcc_hi
	v_cmp_ne_u32_e32 vcc, 0, v169
	v_cndmask_b32_e64 v2, v2, v11, s[12:13]
	v_cndmask_b32_e64 v9, v9, v12, s[12:13]
	v_mov_b32_e32 v11, vcc_hi
	v_mov_b32_e32 v12, vcc_lo
	v_cndmask_b32_e64 v9, v9, v11, s[14:15]
	v_cndmask_b32_e64 v2, v2, v12, s[14:15]
	v_cmp_ne_u32_e32 vcc, 0, v170
	s_nop 1
	v_mov_b32_e32 v10, vcc_lo
	v_mov_b32_e32 v11, vcc_hi
	v_cmp_ne_u32_e32 vcc, 0, v171
	v_cndmask_b32_e64 v2, v2, v10, s[16:17]
	v_cndmask_b32_e64 v8, v9, v11, s[16:17]
	v_mov_b32_e32 v9, vcc_hi
	v_mov_b32_e32 v10, vcc_lo
	v_cndmask_b32_e64 v9, v8, v9, s[18:19]
	v_cndmask_b32_e64 v8, v2, v10, s[18:19]
	s_mov_b64 s[2:3], exec
	s_mov_b64 exec, s[0:1]
	global_store_dwordx2 v[4:5], v[8:9], off
	s_mov_b64 exec, s[2:3]
	v_cmp_ne_u64_e32 vcc, 0, v[8:9]
	s_and_b64 s[20:21], s[0:1], vcc
	s_cmp_lg_u64 s[20:21], 0
	s_cselect_b32 s20, 256, 0
	s_or_b32 s76, s76, s20
	v_cmp_ne_u64_e32 vcc, -1, v[8:9]
	s_and_b64 s[20:21], s[0:1], vcc
	s_cmp_lg_u64 s[20:21], 0
	s_cselect_b32 s20, 256, 0
	s_or_b32 s77, s77, s20
	v_lshl_add_u64 v[4:5], v[4:5], 0, 8
	global_load_dword v220, v96, s[60:61] offset:3840 nt
	global_load_dword v221, v96, s[62:63] offset:3840 nt
	global_load_dword v222, v96, s[64:65] offset:3840 nt
	global_load_dword v223, v96, s[66:67] offset:3840 nt
	global_load_dword v224, v96, s[68:69] offset:3840 nt
	global_load_dword v225, v96, s[70:71] offset:3840 nt
	global_load_dword v226, v96, s[72:73] offset:3840 nt
	global_load_dword v227, v96, s[74:75] offset:3840 nt
	s_waitcnt vmcnt(54)
	v_cmp_ne_u32_e32 vcc, 0, v172
	s_nop 1
	v_mov_b32_e32 v2, vcc_lo
	v_mov_b32_e32 v9, vcc_hi
	v_cmp_ne_u32_e32 vcc, 0, v173
	v_cndmask_b32_e64 v2, 0, v2, s[22:23]
	v_cndmask_b32_e64 v9, 0, v9, s[22:23]
	v_mov_b32_e32 v11, vcc_hi
	v_mov_b32_e32 v14, vcc_lo
	v_cndmask_b32_e64 v9, v9, v11, s[6:7]
	v_cndmask_b32_e64 v2, v2, v14, s[6:7]
	v_cmp_ne_u32_e32 vcc, 0, v174
	s_nop 1
	v_mov_b32_e32 v11, vcc_lo
	v_mov_b32_e32 v14, vcc_hi
	v_cmp_ne_u32_e32 vcc, 0, v175
	v_cndmask_b32_e64 v2, v2, v11, s[8:9]
	v_cndmask_b32_e64 v9, v9, v14, s[8:9]
	v_mov_b32_e32 v11, vcc_hi
	v_mov_b32_e32 v14, vcc_lo
	v_cmp_ne_u32_e32 vcc, 0, v176
	v_cndmask_b32_e64 v9, v9, v11, s[10:11]
	v_cndmask_b32_e64 v2, v2, v14, s[10:11]
	v_mov_b32_e32 v11, vcc_lo
	v_mov_b32_e32 v12, vcc_hi
	v_cmp_ne_u32_e32 vcc, 0, v177
	v_cndmask_b32_e64 v2, v2, v11, s[12:13]
	v_cndmask_b32_e64 v9, v9, v12, s[12:13]
	v_mov_b32_e32 v11, vcc_hi
	v_mov_b32_e32 v12, vcc_lo
	v_cndmask_b32_e64 v9, v9, v11, s[14:15]
	v_cndmask_b32_e64 v2, v2, v12, s[14:15]
	v_cmp_ne_u32_e32 vcc, 0, v178
	s_nop 1
	v_mov_b32_e32 v10, vcc_lo
	v_mov_b32_e32 v11, vcc_hi
	v_cmp_ne_u32_e32 vcc, 0, v179
	v_cndmask_b32_e64 v2, v2, v10, s[16:17]
	v_cndmask_b32_e64 v8, v9, v11, s[16:17]
	v_mov_b32_e32 v9, vcc_hi
	v_mov_b32_e32 v10, vcc_lo
	v_cndmask_b32_e64 v9, v8, v9, s[18:19]
	v_cndmask_b32_e64 v8, v2, v10, s[18:19]
	s_mov_b64 s[2:3], exec
	s_mov_b64 exec, s[0:1]
	global_store_dwordx2 v[4:5], v[8:9], off
	s_mov_b64 exec, s[2:3]
	v_cmp_ne_u64_e32 vcc, 0, v[8:9]
	s_and_b64 s[20:21], s[0:1], vcc
	s_cmp_lg_u64 s[20:21], 0
	s_cselect_b32 s20, 512, 0
	s_or_b32 s76, s76, s20
	v_cmp_ne_u64_e32 vcc, -1, v[8:9]
	s_and_b64 s[20:21], s[0:1], vcc
	s_cmp_lg_u64 s[20:21], 0
	s_cselect_b32 s20, 512, 0
	s_or_b32 s77, s77, s20
	v_lshl_add_u64 v[4:5], v[4:5], 0, 8
	s_waitcnt vmcnt(46)
	v_cmp_ne_u32_e32 vcc, 0, v180
	s_nop 1
	v_mov_b32_e32 v2, vcc_lo
	v_mov_b32_e32 v9, vcc_hi
	v_cmp_ne_u32_e32 vcc, 0, v181
	v_cndmask_b32_e64 v2, 0, v2, s[22:23]
	v_cndmask_b32_e64 v9, 0, v9, s[22:23]
	v_mov_b32_e32 v11, vcc_hi
	v_mov_b32_e32 v14, vcc_lo
	v_cndmask_b32_e64 v9, v9, v11, s[6:7]
	v_cndmask_b32_e64 v2, v2, v14, s[6:7]
	v_cmp_ne_u32_e32 vcc, 0, v182
	s_nop 1
	v_mov_b32_e32 v11, vcc_lo
	v_mov_b32_e32 v14, vcc_hi
	v_cmp_ne_u32_e32 vcc, 0, v183
	v_cndmask_b32_e64 v2, v2, v11, s[8:9]
	v_cndmask_b32_e64 v9, v9, v14, s[8:9]
	v_mov_b32_e32 v11, vcc_hi
	v_mov_b32_e32 v14, vcc_lo
	v_cmp_ne_u32_e32 vcc, 0, v184
	v_cndmask_b32_e64 v9, v9, v11, s[10:11]
	v_cndmask_b32_e64 v2, v2, v14, s[10:11]
	v_mov_b32_e32 v11, vcc_lo
	v_mov_b32_e32 v12, vcc_hi
	v_cmp_ne_u32_e32 vcc, 0, v185
	v_cndmask_b32_e64 v2, v2, v11, s[12:13]
	v_cndmask_b32_e64 v9, v9, v12, s[12:13]
	v_mov_b32_e32 v11, vcc_hi
	v_mov_b32_e32 v12, vcc_lo
	v_cndmask_b32_e64 v9, v9, v11, s[14:15]
	v_cndmask_b32_e64 v2, v2, v12, s[14:15]
	v_cmp_ne_u32_e32 vcc, 0, v186
	s_nop 1
	v_mov_b32_e32 v10, vcc_lo
	v_mov_b32_e32 v11, vcc_hi
	v_cmp_ne_u32_e32 vcc, 0, v187
	v_cndmask_b32_e64 v2, v2, v10, s[16:17]
	v_cndmask_b32_e64 v8, v9, v11, s[16:17]
	v_mov_b32_e32 v9, vcc_hi
	v_mov_b32_e32 v10, vcc_lo
	v_cndmask_b32_e64 v9, v8, v9, s[18:19]
	v_cndmask_b32_e64 v8, v2, v10, s[18:19]
	s_mov_b64 s[2:3], exec
	s_mov_b64 exec, s[0:1]
	global_store_dwordx2 v[4:5], v[8:9], off
	s_mov_b64 exec, s[2:3]
	v_cmp_ne_u64_e32 vcc, 0, v[8:9]
	s_and_b64 s[20:21], s[0:1], vcc
	s_cmp_lg_u64 s[20:21], 0
	s_cselect_b32 s20, 1024, 0
	s_or_b32 s76, s76, s20
	v_cmp_ne_u64_e32 vcc, -1, v[8:9]
	s_and_b64 s[20:21], s[0:1], vcc
	s_cmp_lg_u64 s[20:21], 0
	s_cselect_b32 s20, 1024, 0
	s_or_b32 s77, s77, s20
	v_lshl_add_u64 v[4:5], v[4:5], 0, 8
	s_waitcnt vmcnt(38)
	v_cmp_ne_u32_e32 vcc, 0, v188
	s_nop 1
	v_mov_b32_e32 v2, vcc_lo
	v_mov_b32_e32 v9, vcc_hi
	v_cmp_ne_u32_e32 vcc, 0, v189
	v_cndmask_b32_e64 v2, 0, v2, s[22:23]
	v_cndmask_b32_e64 v9, 0, v9, s[22:23]
	v_mov_b32_e32 v11, vcc_hi
	v_mov_b32_e32 v14, vcc_lo
	v_cndmask_b32_e64 v9, v9, v11, s[6:7]
	v_cndmask_b32_e64 v2, v2, v14, s[6:7]
	v_cmp_ne_u32_e32 vcc, 0, v190
	s_nop 1
	v_mov_b32_e32 v11, vcc_lo
	v_mov_b32_e32 v14, vcc_hi
	v_cmp_ne_u32_e32 vcc, 0, v191
	v_cndmask_b32_e64 v2, v2, v11, s[8:9]
	v_cndmask_b32_e64 v9, v9, v14, s[8:9]
	v_mov_b32_e32 v11, vcc_hi
	v_mov_b32_e32 v14, vcc_lo
	v_cmp_ne_u32_e32 vcc, 0, v192
	v_cndmask_b32_e64 v9, v9, v11, s[10:11]
	v_cndmask_b32_e64 v2, v2, v14, s[10:11]
	v_mov_b32_e32 v11, vcc_lo
	v_mov_b32_e32 v12, vcc_hi
	v_cmp_ne_u32_e32 vcc, 0, v193
	v_cndmask_b32_e64 v2, v2, v11, s[12:13]
	v_cndmask_b32_e64 v9, v9, v12, s[12:13]
	v_mov_b32_e32 v11, vcc_hi
	v_mov_b32_e32 v12, vcc_lo
	v_cndmask_b32_e64 v9, v9, v11, s[14:15]
	v_cndmask_b32_e64 v2, v2, v12, s[14:15]
	v_cmp_ne_u32_e32 vcc, 0, v194
	s_nop 1
	v_mov_b32_e32 v10, vcc_lo
	v_mov_b32_e32 v11, vcc_hi
	v_cmp_ne_u32_e32 vcc, 0, v195
	v_cndmask_b32_e64 v2, v2, v10, s[16:17]
	v_cndmask_b32_e64 v8, v9, v11, s[16:17]
	v_mov_b32_e32 v9, vcc_hi
	v_mov_b32_e32 v10, vcc_lo
	v_cndmask_b32_e64 v9, v8, v9, s[18:19]
	v_cndmask_b32_e64 v8, v2, v10, s[18:19]
	s_mov_b64 s[2:3], exec
	s_mov_b64 exec, s[0:1]
	global_store_dwordx2 v[4:5], v[8:9], off
	s_mov_b64 exec, s[2:3]
	v_cmp_ne_u64_e32 vcc, 0, v[8:9]
	s_and_b64 s[20:21], s[0:1], vcc
	s_cmp_lg_u64 s[20:21], 0
	s_cselect_b32 s20, 2048, 0
	s_or_b32 s76, s76, s20
	v_cmp_ne_u64_e32 vcc, -1, v[8:9]
	s_and_b64 s[20:21], s[0:1], vcc
	s_cmp_lg_u64 s[20:21], 0
	s_cselect_b32 s20, 2048, 0
	s_or_b32 s77, s77, s20
	v_lshl_add_u64 v[4:5], v[4:5], 0, 8
	s_waitcnt vmcnt(30)
	v_cmp_ne_u32_e32 vcc, 0, v196
	s_nop 1
	v_mov_b32_e32 v2, vcc_lo
	v_mov_b32_e32 v9, vcc_hi
	v_cmp_ne_u32_e32 vcc, 0, v197
	v_cndmask_b32_e64 v2, 0, v2, s[22:23]
	v_cndmask_b32_e64 v9, 0, v9, s[22:23]
	v_mov_b32_e32 v11, vcc_hi
	v_mov_b32_e32 v14, vcc_lo
	v_cndmask_b32_e64 v9, v9, v11, s[6:7]
	v_cndmask_b32_e64 v2, v2, v14, s[6:7]
	v_cmp_ne_u32_e32 vcc, 0, v198
	s_nop 1
	v_mov_b32_e32 v11, vcc_lo
	v_mov_b32_e32 v14, vcc_hi
	v_cmp_ne_u32_e32 vcc, 0, v199
	v_cndmask_b32_e64 v2, v2, v11, s[8:9]
	v_cndmask_b32_e64 v9, v9, v14, s[8:9]
	v_mov_b32_e32 v11, vcc_hi
	v_mov_b32_e32 v14, vcc_lo
	v_cmp_ne_u32_e32 vcc, 0, v200
	v_cndmask_b32_e64 v9, v9, v11, s[10:11]
	v_cndmask_b32_e64 v2, v2, v14, s[10:11]
	v_mov_b32_e32 v11, vcc_lo
	v_mov_b32_e32 v12, vcc_hi
	v_cmp_ne_u32_e32 vcc, 0, v201
	v_cndmask_b32_e64 v2, v2, v11, s[12:13]
	v_cndmask_b32_e64 v9, v9, v12, s[12:13]
	v_mov_b32_e32 v11, vcc_hi
	v_mov_b32_e32 v12, vcc_lo
	v_cndmask_b32_e64 v9, v9, v11, s[14:15]
	v_cndmask_b32_e64 v2, v2, v12, s[14:15]
	v_cmp_ne_u32_e32 vcc, 0, v202
	s_nop 1
	v_mov_b32_e32 v10, vcc_lo
	v_mov_b32_e32 v11, vcc_hi
	v_cmp_ne_u32_e32 vcc, 0, v203
	v_cndmask_b32_e64 v2, v2, v10, s[16:17]
	v_cndmask_b32_e64 v8, v9, v11, s[16:17]
	v_mov_b32_e32 v9, vcc_hi
	v_mov_b32_e32 v10, vcc_lo
	v_cndmask_b32_e64 v9, v8, v9, s[18:19]
	v_cndmask_b32_e64 v8, v2, v10, s[18:19]
	s_mov_b64 s[2:3], exec
	s_mov_b64 exec, s[0:1]
	global_store_dwordx2 v[4:5], v[8:9], off
	s_mov_b64 exec, s[2:3]
	v_cmp_ne_u64_e32 vcc, 0, v[8:9]
	s_and_b64 s[20:21], s[0:1], vcc
	s_cmp_lg_u64 s[20:21], 0
	s_cselect_b32 s20, 4096, 0
	s_or_b32 s76, s76, s20
	v_cmp_ne_u64_e32 vcc, -1, v[8:9]
	s_and_b64 s[20:21], s[0:1], vcc
	s_cmp_lg_u64 s[20:21], 0
	s_cselect_b32 s20, 4096, 0
	s_or_b32 s77, s77, s20
	v_lshl_add_u64 v[4:5], v[4:5], 0, 8
	s_waitcnt vmcnt(22)
	v_cmp_ne_u32_e32 vcc, 0, v204
	s_nop 1
	v_mov_b32_e32 v2, vcc_lo
	v_mov_b32_e32 v9, vcc_hi
	v_cmp_ne_u32_e32 vcc, 0, v205
	v_cndmask_b32_e64 v2, 0, v2, s[22:23]
	v_cndmask_b32_e64 v9, 0, v9, s[22:23]
	v_mov_b32_e32 v11, vcc_hi
	v_mov_b32_e32 v14, vcc_lo
	v_cndmask_b32_e64 v9, v9, v11, s[6:7]
	v_cndmask_b32_e64 v2, v2, v14, s[6:7]
	v_cmp_ne_u32_e32 vcc, 0, v206
	s_nop 1
	v_mov_b32_e32 v11, vcc_lo
	v_mov_b32_e32 v14, vcc_hi
	v_cmp_ne_u32_e32 vcc, 0, v207
	v_cndmask_b32_e64 v2, v2, v11, s[8:9]
	v_cndmask_b32_e64 v9, v9, v14, s[8:9]
	v_mov_b32_e32 v11, vcc_hi
	v_mov_b32_e32 v14, vcc_lo
	v_cmp_ne_u32_e32 vcc, 0, v208
	v_cndmask_b32_e64 v9, v9, v11, s[10:11]
	v_cndmask_b32_e64 v2, v2, v14, s[10:11]
	v_mov_b32_e32 v11, vcc_lo
	v_mov_b32_e32 v12, vcc_hi
	v_cmp_ne_u32_e32 vcc, 0, v209
	v_cndmask_b32_e64 v2, v2, v11, s[12:13]
	v_cndmask_b32_e64 v9, v9, v12, s[12:13]
	v_mov_b32_e32 v11, vcc_hi
	v_mov_b32_e32 v12, vcc_lo
	v_cndmask_b32_e64 v9, v9, v11, s[14:15]
	v_cndmask_b32_e64 v2, v2, v12, s[14:15]
	v_cmp_ne_u32_e32 vcc, 0, v210
	s_nop 1
	v_mov_b32_e32 v10, vcc_lo
	v_mov_b32_e32 v11, vcc_hi
	v_cmp_ne_u32_e32 vcc, 0, v211
	v_cndmask_b32_e64 v2, v2, v10, s[16:17]
	v_cndmask_b32_e64 v8, v9, v11, s[16:17]
	v_mov_b32_e32 v9, vcc_hi
	v_mov_b32_e32 v10, vcc_lo
	v_cndmask_b32_e64 v9, v8, v9, s[18:19]
	v_cndmask_b32_e64 v8, v2, v10, s[18:19]
	s_mov_b64 s[2:3], exec
	s_mov_b64 exec, s[0:1]
	global_store_dwordx2 v[4:5], v[8:9], off
	s_mov_b64 exec, s[2:3]
	v_cmp_ne_u64_e32 vcc, 0, v[8:9]
	s_and_b64 s[20:21], s[0:1], vcc
	s_cmp_lg_u64 s[20:21], 0
	s_cselect_b32 s20, 8192, 0
	s_or_b32 s76, s76, s20
	v_cmp_ne_u64_e32 vcc, -1, v[8:9]
	s_and_b64 s[20:21], s[0:1], vcc
	s_cmp_lg_u64 s[20:21], 0
	s_cselect_b32 s20, 8192, 0
	s_or_b32 s77, s77, s20
	v_lshl_add_u64 v[4:5], v[4:5], 0, 8
	s_waitcnt vmcnt(14)
	v_cmp_ne_u32_e32 vcc, 0, v212
	s_nop 1
	v_mov_b32_e32 v2, vcc_lo
	v_mov_b32_e32 v9, vcc_hi
	v_cmp_ne_u32_e32 vcc, 0, v213
	v_cndmask_b32_e64 v2, 0, v2, s[22:23]
	v_cndmask_b32_e64 v9, 0, v9, s[22:23]
	v_mov_b32_e32 v11, vcc_hi
	v_mov_b32_e32 v14, vcc_lo
	v_cndmask_b32_e64 v9, v9, v11, s[6:7]
	v_cndmask_b32_e64 v2, v2, v14, s[6:7]
	v_cmp_ne_u32_e32 vcc, 0, v214
	s_nop 1
	v_mov_b32_e32 v11, vcc_lo
	v_mov_b32_e32 v14, vcc_hi
	v_cmp_ne_u32_e32 vcc, 0, v215
	v_cndmask_b32_e64 v2, v2, v11, s[8:9]
	v_cndmask_b32_e64 v9, v9, v14, s[8:9]
	v_mov_b32_e32 v11, vcc_hi
	v_mov_b32_e32 v14, vcc_lo
	v_cmp_ne_u32_e32 vcc, 0, v216
	v_cndmask_b32_e64 v9, v9, v11, s[10:11]
	v_cndmask_b32_e64 v2, v2, v14, s[10:11]
	v_mov_b32_e32 v11, vcc_lo
	v_mov_b32_e32 v12, vcc_hi
	v_cmp_ne_u32_e32 vcc, 0, v217
	v_cndmask_b32_e64 v2, v2, v11, s[12:13]
	v_cndmask_b32_e64 v9, v9, v12, s[12:13]
	v_mov_b32_e32 v11, vcc_hi
	v_mov_b32_e32 v12, vcc_lo
	v_cndmask_b32_e64 v9, v9, v11, s[14:15]
	v_cndmask_b32_e64 v2, v2, v12, s[14:15]
	v_cmp_ne_u32_e32 vcc, 0, v218
	s_nop 1
	v_mov_b32_e32 v10, vcc_lo
	v_mov_b32_e32 v11, vcc_hi
	v_cmp_ne_u32_e32 vcc, 0, v219
	v_cndmask_b32_e64 v2, v2, v10, s[16:17]
	v_cndmask_b32_e64 v8, v9, v11, s[16:17]
	v_mov_b32_e32 v9, vcc_hi
	v_mov_b32_e32 v10, vcc_lo
	v_cndmask_b32_e64 v9, v8, v9, s[18:19]
	v_cndmask_b32_e64 v8, v2, v10, s[18:19]
	s_mov_b64 s[2:3], exec
	s_mov_b64 exec, s[0:1]
	global_store_dwordx2 v[4:5], v[8:9], off
	s_mov_b64 exec, s[2:3]
	v_cmp_ne_u64_e32 vcc, 0, v[8:9]
	s_and_b64 s[20:21], s[0:1], vcc
	s_cmp_lg_u64 s[20:21], 0
	s_cselect_b32 s20, 16384, 0
	s_or_b32 s76, s76, s20
	v_cmp_ne_u64_e32 vcc, -1, v[8:9]
	s_and_b64 s[20:21], s[0:1], vcc
	s_cmp_lg_u64 s[20:21], 0
	s_cselect_b32 s20, 16384, 0
	s_or_b32 s77, s77, s20
	v_lshl_add_u64 v[4:5], v[4:5], 0, 8
	s_waitcnt vmcnt(6)
	v_cmp_ne_u32_e32 vcc, 0, v220
	s_nop 1
	v_mov_b32_e32 v2, vcc_lo
	v_mov_b32_e32 v9, vcc_hi
	v_cmp_ne_u32_e32 vcc, 0, v221
	v_cndmask_b32_e64 v2, 0, v2, s[22:23]
	v_cndmask_b32_e64 v9, 0, v9, s[22:23]
	v_mov_b32_e32 v11, vcc_hi
	v_mov_b32_e32 v14, vcc_lo
	v_cndmask_b32_e64 v9, v9, v11, s[6:7]
	v_cndmask_b32_e64 v2, v2, v14, s[6:7]
	v_cmp_ne_u32_e32 vcc, 0, v222
	s_nop 1
	v_mov_b32_e32 v11, vcc_lo
	v_mov_b32_e32 v14, vcc_hi
	v_cmp_ne_u32_e32 vcc, 0, v223
	v_cndmask_b32_e64 v2, v2, v11, s[8:9]
	v_cndmask_b32_e64 v9, v9, v14, s[8:9]
	v_mov_b32_e32 v11, vcc_hi
	v_mov_b32_e32 v14, vcc_lo
	v_cmp_ne_u32_e32 vcc, 0, v224
	v_cndmask_b32_e64 v9, v9, v11, s[10:11]
	v_cndmask_b32_e64 v2, v2, v14, s[10:11]
	v_mov_b32_e32 v11, vcc_lo
	v_mov_b32_e32 v12, vcc_hi
	v_cmp_ne_u32_e32 vcc, 0, v225
	v_cndmask_b32_e64 v2, v2, v11, s[12:13]
	v_cndmask_b32_e64 v9, v9, v12, s[12:13]
	v_mov_b32_e32 v11, vcc_hi
	v_mov_b32_e32 v12, vcc_lo
	v_cndmask_b32_e64 v9, v9, v11, s[14:15]
	v_cndmask_b32_e64 v2, v2, v12, s[14:15]
	v_cmp_ne_u32_e32 vcc, 0, v226
	s_nop 1
	v_mov_b32_e32 v10, vcc_lo
	v_mov_b32_e32 v11, vcc_hi
	v_cmp_ne_u32_e32 vcc, 0, v227
	v_cndmask_b32_e64 v2, v2, v10, s[16:17]
	v_cndmask_b32_e64 v8, v9, v11, s[16:17]
	v_mov_b32_e32 v9, vcc_hi
	v_mov_b32_e32 v10, vcc_lo
	v_cndmask_b32_e64 v9, v8, v9, s[18:19]
	v_cndmask_b32_e64 v8, v2, v10, s[18:19]
	s_mov_b64 s[2:3], exec
	s_mov_b64 exec, s[0:1]
	global_store_dwordx2 v[4:5], v[8:9], off
	s_mov_b64 exec, s[2:3]
	v_cmp_ne_u64_e32 vcc, 0, v[8:9]
	s_and_b64 s[20:21], s[0:1], vcc
	s_cmp_lg_u64 s[20:21], 0
	s_cselect_b32 s20, 32768, 0
	s_or_b32 s76, s76, s20
	v_cmp_ne_u64_e32 vcc, -1, v[8:9]
	s_and_b64 s[20:21], s[0:1], vcc
	s_cmp_lg_u64 s[20:21], 0
	s_cselect_b32 s20, 32768, 0
	s_or_b32 s77, s77, s20
	v_lshl_add_u64 v[4:5], v[4:5], 0, 8
	v_mov_b32_e32 v2, s76
	v_mov_b32_e32 v8, s77
	s_mov_b64 s[2:3], exec
	s_mov_b64 exec, s[22:23]
	ds_write2_b32 v1, v2, v8 offset1:8
	s_mov_b64 exec, s[2:3]
	s_waitcnt lgkmcnt(0)
	s_barrier
	ds_read_b128 v[8:11], v3
	ds_read_b128 v[12:15], v3 offset:16
	ds_read_b128 v[16:19], v3 offset:32
	ds_read_b128 v[20:23], v3 offset:48
	s_waitcnt lgkmcnt(0)
	v_or_b32_e32 v8, v8, v9
	v_or3_b32 v8, v8, v10, v11
	v_or3_b32 v8, v8, v12, v13
	v_or3_b32 v8, v8, v14, v15
	v_or_b32_e32 v16, v16, v17
	v_or3_b32 v16, v16, v18, v19
	v_or3_b32 v16, v16, v20, v21
	v_or3_b32 v16, v16, v22, v23
	v_and_b32_e32 v2, 15, v0
	v_lshrrev_b32_e32 v8, v2, v8
	v_and_b32_e32 v8, 1, v8
	v_lshrrev_b32_e32 v16, v2, v16
	v_and_b32_e32 v16, 1, v16
	v_lshl_or_b32 v8, v16, 1, v8
	v_lshlrev_b32_e32 v2, 2, v2
	v_cmp_gt_u32_e32 vcc, 16, v0
	s_and_saveexec_b64 s[2:3], vcc
	global_store_dword v2, v8, s[26:27]
	s_mov_b64 exec, s[2:3]

.LBB1_40:
	v_add_u32_e32 v2, s0, v18
	v_and_b32_e32 v20, 32, v19
	v_ashrrev_i32_e32 v21, 8, v19
	v_and_b32_e32 v22, 0x7c0, v16
	v_add_u32_e32 v23, s0, v14
	v_lshrrev_b32_e32 v34, 7, v2
	v_bitop3_b32 v20, v2, v20, 48 bitop3:0x6c
	v_and_b32_e32 v24, 32, v15
	v_ashrrev_i32_e32 v25, 8, v15
	v_lshrrev_b32_e32 v35, 5, v2
	v_lshrrev_b32_e32 v36, 9, v2
	v_bfe_u32 v37, v2, 6, 2
	v_and_b32_e32 v21, 0xffffff80, v21
	v_lshlrev_b32_e32 v2, 2, v22
	v_lshrrev_b32_e32 v22, 7, v23
	v_lshrrev_b32_e32 v20, 1, v20
	v_and_b32_e32 v34, 0x60, v34
	v_add_u32_e32 v26, s0, v10
	v_lshrrev_b32_e32 v38, 5, v23
	v_bitop3_b32 v24, v23, v24, 48 bitop3:0x6c
	v_lshrrev_b32_e32 v39, 9, v23
	v_bfe_u32 v23, v23, 6, 2
	v_and_b32_e32 v25, 0xffffff80, v25
	v_and_b32_e32 v47, 24, v35
	v_and_b32_e32 v36, 4, v36
	v_and_b32_e32 v22, 0x60, v22
	v_and_or_b32 v35, v35, 32, v20
	v_or3_b32 v20, v37, v21, v34
	v_and_b32_e32 v27, 32, v11
	v_ashrrev_i32_e32 v28, 8, v11
	v_lshrrev_b32_e32 v41, 7, v26
	v_and_b32_e32 v48, 24, v38
	v_and_b32_e32 v39, 4, v39
	v_or3_b32 v21, v23, v25, v22
	v_or3_b32 v20, v20, v36, v47
	v_add_u32_e32 v29, s0, v6
	v_lshrrev_b32_e32 v42, 5, v26
	v_bitop3_b32 v27, v26, v27, 48 bitop3:0x6c
	v_lshrrev_b32_e32 v43, 9, v26
	v_bfe_u32 v26, v26, 6, 2
	v_and_b32_e32 v28, 0xffffff80, v28
	v_and_b32_e32 v41, 0x60, v41
	v_or3_b32 v22, v21, v39, v48
	v_ashrrev_i32_e32 v21, 31, v20
	v_and_b32_e32 v30, 32, v7
	v_ashrrev_i32_e32 v31, 8, v7
	v_lshrrev_b32_e32 v44, 7, v29
	v_lshrrev_b32_e32 v24, 1, v24
	v_and_b32_e32 v49, 24, v42
	v_and_b32_e32 v43, 4, v43
	v_or3_b32 v23, v26, v28, v41
	v_lshlrev_b64 v[20:21], 13, v[20:21]
	v_lshrrev_b32_e32 v45, 5, v29
	v_bitop3_b32 v30, v29, v30, 48 bitop3:0x6c
	v_lshrrev_b32_e32 v46, 9, v29
	v_bfe_u32 v29, v29, 6, 2
	v_and_b32_e32 v31, 0xffffff80, v31
	v_and_b32_e32 v44, 0x60, v44
	v_and_or_b32 v34, v38, 32, v24
	v_or3_b32 v24, v23, v43, v49
	v_ashrrev_i32_e32 v23, 31, v22
	v_lshl_add_u64 v[20:21], s[38:39], 0, v[20:21]
	v_and_b32_e32 v32, 0x7c0, v12
	v_lshrrev_b32_e32 v30, 1, v30
	v_and_b32_e32 v50, 24, v45
	v_and_b32_e32 v46, 4, v46
	v_or3_b32 v25, v29, v31, v44
	v_lshlrev_b64 v[22:23], 13, v[22:23]
	v_lshl_add_u64 v[20:21], v[20:21], 0, v[2:3]
	v_lshlrev_b32_e32 v2, 2, v35
	v_and_or_b32 v51, v45, 32, v30
	v_or3_b32 v26, v25, v46, v50
	v_ashrrev_i32_e32 v25, 31, v24
	v_lshl_add_u64 v[28:29], s[38:39], 0, v[22:23]
	v_lshl_add_u64 v[30:31], v[20:21], 0, v[2:3]
	v_lshlrev_b32_e32 v2, 2, v32
	v_and_b32_e32 v33, 0x7c0, v8
	v_lshrrev_b32_e32 v27, 1, v27
	v_lshlrev_b64 v[24:25], 13, v[24:25]
	v_lshl_add_u64 v[28:29], v[28:29], 0, v[2:3]
	v_lshlrev_b32_e32 v2, 2, v34
	v_and_or_b32 v42, v42, 32, v27
	v_ashrrev_i32_e32 v27, 31, v26
	v_lshl_add_u64 v[36:37], s[38:39], 0, v[24:25]
	v_lshl_add_u64 v[38:39], v[28:29], 0, v[2:3]
	v_lshlrev_b32_e32 v2, 2, v33
	v_and_b32_e32 v40, 0x7c0, v0
	v_lshlrev_b64 v[26:27], 13, v[26:27]
	v_lshl_add_u64 v[36:37], v[36:37], 0, v[2:3]
	v_lshlrev_b32_e32 v2, 2, v42
	v_lshl_add_u64 v[44:45], s[38:39], 0, v[26:27]
	global_load_dwordx4 v[20:23], v[30:31], off nt
	global_load_dwordx4 v[24:27], v[30:31], off offset:16 nt
	v_lshl_add_u64 v[46:47], v[36:37], 0, v[2:3]
	v_lshlrev_b32_e32 v2, 2, v40
	global_load_dwordx4 v[28:31], v[38:39], off offset:16 nt
	global_load_dwordx4 v[32:35], v[38:39], off nt
	v_lshl_add_u64 v[44:45], v[44:45], 0, v[2:3]
	v_lshlrev_b32_e32 v2, 2, v51
	global_load_dwordx4 v[36:39], v[46:47], off nt
	global_load_dwordx4 v[40:43], v[46:47], off offset:16 nt
	v_lshl_add_u64 v[52:53], v[44:45], 0, v[2:3]
	global_load_dwordx4 v[44:47], v[52:53], off nt
	global_load_dwordx4 v[48:51], v[52:53], off offset:16 nt
	v_lshl_add_u64 v[52:53], v[4:5], 0, s[0:1]
	v_add_co_u32_e32 v54, vcc, s4, v52
	s_add_u32 s0, s0, 0x8000
	s_nop 0
	v_addc_co_u32_e32 v55, vcc, 0, v53, vcc
	v_add_co_u32_e32 v56, vcc, s5, v52
	s_addc_u32 s1, s1, 0
	s_nop 0
	v_addc_co_u32_e32 v57, vcc, 0, v53, vcc
	v_add_co_u32_e32 v58, vcc, s6, v52
	v_lshl_add_u64 v[0:1], v[0:1], 0, s[2:3]
	v_add_u32_e32 v7, 0x800, v7
	v_lshl_add_u64 v[8:9], v[8:9], 0, s[2:3]
	v_add_u32_e32 v11, 0x800, v11
	v_lshl_add_u64 v[12:13], v[12:13], 0, s[2:3]
	v_add_u32_e32 v15, 0x800, v15
	v_lshl_add_u64 v[16:17], v[16:17], 0, s[2:3]
	v_add_u32_e32 v19, 0x800, v19
	v_addc_co_u32_e32 v59, vcc, 0, v53, vcc
	v_add_u32_e32 v2, s0, v18
	v_and_b32_e32 v60, 32, v19
	v_ashrrev_i32_e32 v61, 8, v19
	v_and_b32_e32 v62, 0x7c0, v16
	v_add_u32_e32 v63, s0, v14
	v_lshrrev_b32_e32 v74, 7, v2
	v_bitop3_b32 v60, v2, v60, 48 bitop3:0x6c
	v_and_b32_e32 v64, 32, v15
	v_ashrrev_i32_e32 v65, 8, v15
	v_lshrrev_b32_e32 v75, 5, v2
	v_lshrrev_b32_e32 v76, 9, v2
	v_bfe_u32 v77, v2, 6, 2
	v_and_b32_e32 v61, 0xffffff80, v61
	v_lshlrev_b32_e32 v2, 2, v62
	v_lshrrev_b32_e32 v62, 7, v63
	v_lshrrev_b32_e32 v60, 1, v60
	v_and_b32_e32 v74, 0x60, v74
	v_add_u32_e32 v66, s0, v10
	v_lshrrev_b32_e32 v78, 5, v63
	v_bitop3_b32 v64, v63, v64, 48 bitop3:0x6c
	v_lshrrev_b32_e32 v79, 9, v63
	v_bfe_u32 v63, v63, 6, 2
	v_and_b32_e32 v65, 0xffffff80, v65
	v_and_b32_e32 v87, 24, v75
	v_and_b32_e32 v76, 4, v76
	v_and_b32_e32 v62, 0x60, v62
	v_and_or_b32 v75, v75, 32, v60
	v_or3_b32 v60, v77, v61, v74
	v_and_b32_e32 v67, 32, v11
	v_ashrrev_i32_e32 v68, 8, v11
	v_lshrrev_b32_e32 v81, 7, v66
	v_and_b32_e32 v88, 24, v78
	v_and_b32_e32 v79, 4, v79
	v_or3_b32 v61, v63, v65, v62
	v_or3_b32 v60, v60, v76, v87
	v_add_u32_e32 v69, s0, v6
	v_lshrrev_b32_e32 v82, 5, v66
	v_bitop3_b32 v67, v66, v67, 48 bitop3:0x6c
	v_lshrrev_b32_e32 v83, 9, v66
	v_bfe_u32 v66, v66, 6, 2
	v_and_b32_e32 v68, 0xffffff80, v68
	v_and_b32_e32 v81, 0x60, v81
	v_or3_b32 v62, v61, v79, v88
	v_ashrrev_i32_e32 v61, 31, v60
	v_and_b32_e32 v70, 32, v7
	v_ashrrev_i32_e32 v71, 8, v7
	v_lshrrev_b32_e32 v84, 7, v69
	v_lshrrev_b32_e32 v64, 1, v64
	v_and_b32_e32 v89, 24, v82
	v_and_b32_e32 v83, 4, v83
	v_or3_b32 v63, v66, v68, v81
	v_lshlrev_b64 v[60:61], 13, v[60:61]
	v_lshrrev_b32_e32 v85, 5, v69
	v_bitop3_b32 v70, v69, v70, 48 bitop3:0x6c
	v_lshrrev_b32_e32 v86, 9, v69
	v_bfe_u32 v69, v69, 6, 2
	v_and_b32_e32 v71, 0xffffff80, v71
	v_and_b32_e32 v84, 0x60, v84
	v_and_or_b32 v74, v78, 32, v64
	v_or3_b32 v64, v63, v83, v89
	v_ashrrev_i32_e32 v63, 31, v62
	v_lshl_add_u64 v[60:61], s[38:39], 0, v[60:61]
	v_and_b32_e32 v72, 0x7c0, v12
	v_lshrrev_b32_e32 v70, 1, v70
	v_and_b32_e32 v90, 24, v85
	v_and_b32_e32 v86, 4, v86
	v_or3_b32 v65, v69, v71, v84
	v_lshlrev_b64 v[62:63], 13, v[62:63]
	v_lshl_add_u64 v[60:61], v[60:61], 0, v[2:3]
	v_lshlrev_b32_e32 v2, 2, v75
	v_and_or_b32 v91, v85, 32, v70
	v_or3_b32 v66, v65, v86, v90
	v_ashrrev_i32_e32 v65, 31, v64
	v_lshl_add_u64 v[68:69], s[38:39], 0, v[62:63]
	v_lshl_add_u64 v[70:71], v[60:61], 0, v[2:3]
	v_lshlrev_b32_e32 v2, 2, v72
	v_and_b32_e32 v73, 0x7c0, v8
	v_lshrrev_b32_e32 v67, 1, v67
	v_lshlrev_b64 v[64:65], 13, v[64:65]
	v_lshl_add_u64 v[68:69], v[68:69], 0, v[2:3]
	v_lshlrev_b32_e32 v2, 2, v74
	v_and_or_b32 v82, v82, 32, v67
	v_ashrrev_i32_e32 v67, 31, v66
	v_lshl_add_u64 v[76:77], s[38:39], 0, v[64:65]
	v_lshl_add_u64 v[78:79], v[68:69], 0, v[2:3]
	v_lshlrev_b32_e32 v2, 2, v73
	v_and_b32_e32 v80, 0x7c0, v0
	v_lshlrev_b64 v[66:67], 13, v[66:67]
	v_lshl_add_u64 v[76:77], v[76:77], 0, v[2:3]
	v_lshlrev_b32_e32 v2, 2, v82
	v_lshl_add_u64 v[84:85], s[38:39], 0, v[66:67]
	global_load_dwordx4 v[60:63], v[70:71], off nt
	global_load_dwordx4 v[64:67], v[70:71], off offset:16 nt
	v_lshl_add_u64 v[86:87], v[76:77], 0, v[2:3]
	v_lshlrev_b32_e32 v2, 2, v80
	global_load_dwordx4 v[68:71], v[78:79], off offset:16 nt
	global_load_dwordx4 v[72:75], v[78:79], off nt
	v_lshl_add_u64 v[84:85], v[84:85], 0, v[2:3]
	v_lshlrev_b32_e32 v2, 2, v91
	global_load_dwordx4 v[76:79], v[86:87], off nt
	global_load_dwordx4 v[80:83], v[86:87], off offset:16 nt
	v_lshl_add_u64 v[92:93], v[84:85], 0, v[2:3]
	global_load_dwordx4 v[84:87], v[92:93], off nt
	global_load_dwordx4 v[88:91], v[92:93], off offset:16 nt
	v_lshl_add_u64 v[92:93], v[4:5], 0, s[0:1]
	v_add_co_u32_e32 v94, vcc, s4, v92
	s_add_u32 s0, s0, 0x8000
	s_nop 0
	v_addc_co_u32_e32 v95, vcc, 0, v93, vcc
	v_add_co_u32_e32 v96, vcc, s5, v92
	s_addc_u32 s1, s1, 0
	s_nop 0
	v_addc_co_u32_e32 v97, vcc, 0, v93, vcc
	v_add_co_u32_e32 v98, vcc, s6, v92
	v_lshl_add_u64 v[0:1], v[0:1], 0, s[2:3]
	v_add_u32_e32 v7, 0x800, v7
	v_lshl_add_u64 v[8:9], v[8:9], 0, s[2:3]
	v_add_u32_e32 v11, 0x800, v11
	v_lshl_add_u64 v[12:13], v[12:13], 0, s[2:3]
	v_add_u32_e32 v15, 0x800, v15
	v_lshl_add_u64 v[16:17], v[16:17], 0, s[2:3]
	v_add_u32_e32 v19, 0x800, v19
	v_addc_co_u32_e32 v99, vcc, 0, v93, vcc
	v_add_u32_e32 v2, s0, v18
	v_and_b32_e32 v100, 32, v19
	v_ashrrev_i32_e32 v101, 8, v19
	v_and_b32_e32 v102, 0x7c0, v16
	v_add_u32_e32 v103, s0, v14
	v_lshrrev_b32_e32 v114, 7, v2
	v_bitop3_b32 v100, v2, v100, 48 bitop3:0x6c
	v_and_b32_e32 v104, 32, v15
	v_ashrrev_i32_e32 v105, 8, v15
	v_lshrrev_b32_e32 v115, 5, v2
	v_lshrrev_b32_e32 v116, 9, v2
	v_bfe_u32 v117, v2, 6, 2
	v_and_b32_e32 v101, 0xffffff80, v101
	v_lshlrev_b32_e32 v2, 2, v102
	v_lshrrev_b32_e32 v102, 7, v103
	v_lshrrev_b32_e32 v100, 1, v100
	v_and_b32_e32 v114, 0x60, v114
	v_add_u32_e32 v106, s0, v10
	v_lshrrev_b32_e32 v118, 5, v103
	v_bitop3_b32 v104, v103, v104, 48 bitop3:0x6c
	v_lshrrev_b32_e32 v119, 9, v103
	v_bfe_u32 v103, v103, 6, 2
	v_and_b32_e32 v105, 0xffffff80, v105
	v_and_b32_e32 v127, 24, v115
	v_and_b32_e32 v116, 4, v116
	v_and_b32_e32 v102, 0x60, v102
	v_and_or_b32 v115, v115, 32, v100
	v_or3_b32 v100, v117, v101, v114
	v_and_b32_e32 v107, 32, v11
	v_ashrrev_i32_e32 v108, 8, v11
	v_lshrrev_b32_e32 v121, 7, v106
	v_and_b32_e32 v128, 24, v118
	v_and_b32_e32 v119, 4, v119
	v_or3_b32 v101, v103, v105, v102
	v_or3_b32 v100, v100, v116, v127
	v_add_u32_e32 v109, s0, v6
	v_lshrrev_b32_e32 v122, 5, v106
	v_bitop3_b32 v107, v106, v107, 48 bitop3:0x6c
	v_lshrrev_b32_e32 v123, 9, v106
	v_bfe_u32 v106, v106, 6, 2
	v_and_b32_e32 v108, 0xffffff80, v108
	v_and_b32_e32 v121, 0x60, v121
	v_or3_b32 v102, v101, v119, v128
	v_ashrrev_i32_e32 v101, 31, v100
	v_and_b32_e32 v110, 32, v7
	v_ashrrev_i32_e32 v111, 8, v7
	v_lshrrev_b32_e32 v124, 7, v109
	v_lshrrev_b32_e32 v104, 1, v104
	v_and_b32_e32 v129, 24, v122
	v_and_b32_e32 v123, 4, v123
	v_or3_b32 v103, v106, v108, v121
	v_lshlrev_b64 v[100:101], 13, v[100:101]
	v_lshrrev_b32_e32 v125, 5, v109
	v_bitop3_b32 v110, v109, v110, 48 bitop3:0x6c
	v_lshrrev_b32_e32 v126, 9, v109
	v_bfe_u32 v109, v109, 6, 2
	v_and_b32_e32 v111, 0xffffff80, v111
	v_and_b32_e32 v124, 0x60, v124
	v_and_or_b32 v114, v118, 32, v104
	v_or3_b32 v104, v103, v123, v129
	v_ashrrev_i32_e32 v103, 31, v102
	v_lshl_add_u64 v[100:101], s[38:39], 0, v[100:101]
	v_and_b32_e32 v112, 0x7c0, v12
	v_lshrrev_b32_e32 v110, 1, v110
	v_and_b32_e32 v130, 24, v125
	v_and_b32_e32 v126, 4, v126
	v_or3_b32 v105, v109, v111, v124
	v_lshlrev_b64 v[102:103], 13, v[102:103]
	v_lshl_add_u64 v[100:101], v[100:101], 0, v[2:3]
	v_lshlrev_b32_e32 v2, 2, v115
	v_and_or_b32 v131, v125, 32, v110
	v_or3_b32 v106, v105, v126, v130
	v_ashrrev_i32_e32 v105, 31, v104
	v_lshl_add_u64 v[108:109], s[38:39], 0, v[102:103]
	v_lshl_add_u64 v[110:111], v[100:101], 0, v[2:3]
	v_lshlrev_b32_e32 v2, 2, v112
	v_and_b32_e32 v113, 0x7c0, v8
	v_lshrrev_b32_e32 v107, 1, v107
	v_lshlrev_b64 v[104:105], 13, v[104:105]
	v_lshl_add_u64 v[108:109], v[108:109], 0, v[2:3]
	v_lshlrev_b32_e32 v2, 2, v114
	v_and_or_b32 v122, v122, 32, v107
	v_ashrrev_i32_e32 v107, 31, v106
	v_lshl_add_u64 v[116:117], s[38:39], 0, v[104:105]
	v_lshl_add_u64 v[118:119], v[108:109], 0, v[2:3]
	v_lshlrev_b32_e32 v2, 2, v113
	v_and_b32_e32 v120, 0x7c0, v0
	v_lshlrev_b64 v[106:107], 13, v[106:107]
	v_lshl_add_u64 v[116:117], v[116:117], 0, v[2:3]
	v_lshlrev_b32_e32 v2, 2, v122
	v_lshl_add_u64 v[124:125], s[38:39], 0, v[106:107]
	global_load_dwordx4 v[100:103], v[110:111], off nt
	global_load_dwordx4 v[104:107], v[110:111], off offset:16 nt
	v_lshl_add_u64 v[126:127], v[116:117], 0, v[2:3]
	v_lshlrev_b32_e32 v2, 2, v120
	global_load_dwordx4 v[108:111], v[118:119], off offset:16 nt
	global_load_dwordx4 v[112:115], v[118:119], off nt
	v_lshl_add_u64 v[124:125], v[124:125], 0, v[2:3]
	v_lshlrev_b32_e32 v2, 2, v131
	global_load_dwordx4 v[116:119], v[126:127], off nt
	global_load_dwordx4 v[120:123], v[126:127], off offset:16 nt
	v_lshl_add_u64 v[132:133], v[124:125], 0, v[2:3]
	global_load_dwordx4 v[124:127], v[132:133], off nt
	global_load_dwordx4 v[128:131], v[132:133], off offset:16 nt
	v_lshl_add_u64 v[132:133], v[4:5], 0, s[0:1]
	v_add_co_u32_e32 v134, vcc, s4, v132
	s_add_u32 s0, s0, 0x8000
	s_nop 0
	v_addc_co_u32_e32 v135, vcc, 0, v133, vcc
	v_add_co_u32_e32 v136, vcc, s5, v132
	s_addc_u32 s1, s1, 0
	s_nop 0
	v_addc_co_u32_e32 v137, vcc, 0, v133, vcc
	v_add_co_u32_e32 v138, vcc, s6, v132
	v_lshl_add_u64 v[0:1], v[0:1], 0, s[2:3]
	v_add_u32_e32 v7, 0x800, v7
	v_lshl_add_u64 v[8:9], v[8:9], 0, s[2:3]
	v_add_u32_e32 v11, 0x800, v11
	v_lshl_add_u64 v[12:13], v[12:13], 0, s[2:3]
	v_add_u32_e32 v15, 0x800, v15
	v_lshl_add_u64 v[16:17], v[16:17], 0, s[2:3]
	v_add_u32_e32 v19, 0x800, v19
	v_addc_co_u32_e32 v139, vcc, 0, v133, vcc
	v_add_u32_e32 v2, s0, v18
	v_and_b32_e32 v140, 32, v19
	v_ashrrev_i32_e32 v141, 8, v19
	v_and_b32_e32 v142, 0x7c0, v16
	v_add_u32_e32 v143, s0, v14
	v_lshrrev_b32_e32 v154, 7, v2
	v_bitop3_b32 v140, v2, v140, 48 bitop3:0x6c
	v_and_b32_e32 v144, 32, v15
	v_ashrrev_i32_e32 v145, 8, v15
	v_lshrrev_b32_e32 v155, 5, v2
	v_lshrrev_b32_e32 v156, 9, v2
	v_bfe_u32 v157, v2, 6, 2
	v_and_b32_e32 v141, 0xffffff80, v141
	v_lshlrev_b32_e32 v2, 2, v142
	v_lshrrev_b32_e32 v142, 7, v143
	v_lshrrev_b32_e32 v140, 1, v140
	v_and_b32_e32 v154, 0x60, v154
	v_add_u32_e32 v146, s0, v10
	v_lshrrev_b32_e32 v158, 5, v143
	v_bitop3_b32 v144, v143, v144, 48 bitop3:0x6c
	v_lshrrev_b32_e32 v159, 9, v143
	v_bfe_u32 v143, v143, 6, 2
	v_and_b32_e32 v145, 0xffffff80, v145
	v_and_b32_e32 v167, 24, v155
	v_and_b32_e32 v156, 4, v156
	v_and_b32_e32 v142, 0x60, v142
	v_and_or_b32 v155, v155, 32, v140
	v_or3_b32 v140, v157, v141, v154
	v_and_b32_e32 v147, 32, v11
	v_ashrrev_i32_e32 v148, 8, v11
	v_lshrrev_b32_e32 v161, 7, v146
	v_and_b32_e32 v168, 24, v158
	v_and_b32_e32 v159, 4, v159
	v_or3_b32 v141, v143, v145, v142
	v_or3_b32 v140, v140, v156, v167
	v_add_u32_e32 v149, s0, v6
	v_lshrrev_b32_e32 v162, 5, v146
	v_bitop3_b32 v147, v146, v147, 48 bitop3:0x6c
	v_lshrrev_b32_e32 v163, 9, v146
	v_bfe_u32 v146, v146, 6, 2
	v_and_b32_e32 v148, 0xffffff80, v148
	v_and_b32_e32 v161, 0x60, v161
	v_or3_b32 v142, v141, v159, v168
	v_ashrrev_i32_e32 v141, 31, v140
	v_and_b32_e32 v150, 32, v7
	v_ashrrev_i32_e32 v151, 8, v7
	v_lshrrev_b32_e32 v164, 7, v149
	v_lshrrev_b32_e32 v144, 1, v144
	v_and_b32_e32 v169, 24, v162
	v_and_b32_e32 v163, 4, v163
	v_or3_b32 v143, v146, v148, v161
	v_lshlrev_b64 v[140:141], 13, v[140:141]
	v_lshrrev_b32_e32 v165, 5, v149
	v_bitop3_b32 v150, v149, v150, 48 bitop3:0x6c
	v_lshrrev_b32_e32 v166, 9, v149
	v_bfe_u32 v149, v149, 6, 2
	v_and_b32_e32 v151, 0xffffff80, v151
	v_and_b32_e32 v164, 0x60, v164
	v_and_or_b32 v154, v158, 32, v144
	v_or3_b32 v144, v143, v163, v169
	v_ashrrev_i32_e32 v143, 31, v142
	v_lshl_add_u64 v[140:141], s[38:39], 0, v[140:141]
	v_and_b32_e32 v152, 0x7c0, v12
	v_lshrrev_b32_e32 v150, 1, v150
	v_and_b32_e32 v170, 24, v165
	v_and_b32_e32 v166, 4, v166
	v_or3_b32 v145, v149, v151, v164
	v_lshlrev_b64 v[142:143], 13, v[142:143]
	v_lshl_add_u64 v[140:141], v[140:141], 0, v[2:3]
	v_lshlrev_b32_e32 v2, 2, v155
	v_and_or_b32 v171, v165, 32, v150
	v_or3_b32 v146, v145, v166, v170
	v_ashrrev_i32_e32 v145, 31, v144
	v_lshl_add_u64 v[148:149], s[38:39], 0, v[142:143]
	v_lshl_add_u64 v[150:151], v[140:141], 0, v[2:3]
	v_lshlrev_b32_e32 v2, 2, v152
	v_and_b32_e32 v153, 0x7c0, v8
	v_lshrrev_b32_e32 v147, 1, v147
	v_lshlrev_b64 v[144:145], 13, v[144:145]
	v_lshl_add_u64 v[148:149], v[148:149], 0, v[2:3]
	v_lshlrev_b32_e32 v2, 2, v154
	v_and_or_b32 v162, v162, 32, v147
	v_ashrrev_i32_e32 v147, 31, v146
	v_lshl_add_u64 v[156:157], s[38:39], 0, v[144:145]
	v_lshl_add_u64 v[158:159], v[148:149], 0, v[2:3]
	v_lshlrev_b32_e32 v2, 2, v153
	v_and_b32_e32 v160, 0x7c0, v0
	v_lshlrev_b64 v[146:147], 13, v[146:147]
	v_lshl_add_u64 v[156:157], v[156:157], 0, v[2:3]
	v_lshlrev_b32_e32 v2, 2, v162
	v_lshl_add_u64 v[164:165], s[38:39], 0, v[146:147]
	global_load_dwordx4 v[140:143], v[150:151], off nt
	global_load_dwordx4 v[144:147], v[150:151], off offset:16 nt
	v_lshl_add_u64 v[166:167], v[156:157], 0, v[2:3]
	v_lshlrev_b32_e32 v2, 2, v160
	global_load_dwordx4 v[148:151], v[158:159], off offset:16 nt
	global_load_dwordx4 v[152:155], v[158:159], off nt
	v_lshl_add_u64 v[164:165], v[164:165], 0, v[2:3]
	v_lshlrev_b32_e32 v2, 2, v171
	global_load_dwordx4 v[156:159], v[166:167], off nt
	global_load_dwordx4 v[160:163], v[166:167], off offset:16 nt
	v_lshl_add_u64 v[172:173], v[164:165], 0, v[2:3]
	global_load_dwordx4 v[164:167], v[172:173], off nt
	global_load_dwordx4 v[168:171], v[172:173], off offset:16 nt
	v_lshl_add_u64 v[172:173], v[4:5], 0, s[0:1]
	v_add_co_u32_e32 v174, vcc, s4, v172
	s_add_u32 s0, s0, 0x8000
	s_nop 0
	v_addc_co_u32_e32 v175, vcc, 0, v173, vcc
	v_add_co_u32_e32 v176, vcc, s5, v172
	s_addc_u32 s1, s1, 0
	s_nop 0
	v_addc_co_u32_e32 v177, vcc, 0, v173, vcc
	v_add_co_u32_e32 v178, vcc, s6, v172
	v_lshl_add_u64 v[0:1], v[0:1], 0, s[2:3]
	v_add_u32_e32 v7, 0x800, v7
	v_lshl_add_u64 v[8:9], v[8:9], 0, s[2:3]
	v_add_u32_e32 v11, 0x800, v11
	v_lshl_add_u64 v[12:13], v[12:13], 0, s[2:3]
	v_add_u32_e32 v15, 0x800, v15
	v_lshl_add_u64 v[16:17], v[16:17], 0, s[2:3]
	v_add_u32_e32 v19, 0x800, v19
	v_addc_co_u32_e32 v179, vcc, 0, v173, vcc
	s_waitcnt vmcnt(31)
	v_cvt_pk_f16_f32 v20, v20, v21
	v_cvt_pk_f16_f32 v21, v22, v23
	s_waitcnt vmcnt(30)
	v_cvt_pk_f16_f32 v22, v24, v25
	v_cvt_pk_f16_f32 v23, v26, v27
	global_store_dwordx4 v[52:53], v[20:23], off sc1
	s_waitcnt vmcnt(29)
	s_nop 0
	v_cvt_pk_f16_f32 v20, v32, v33
	v_cvt_pk_f16_f32 v21, v34, v35
	v_cvt_pk_f16_f32 v22, v28, v29
	v_cvt_pk_f16_f32 v23, v30, v31
	global_store_dwordx4 v[54:55], v[20:23], off sc1
	s_waitcnt vmcnt(29)
	s_nop 0
	v_cvt_pk_f16_f32 v20, v36, v37
	v_cvt_pk_f16_f32 v21, v38, v39
	s_waitcnt vmcnt(28)
	v_cvt_pk_f16_f32 v22, v40, v41
	v_cvt_pk_f16_f32 v23, v42, v43
	global_store_dwordx4 v[56:57], v[20:23], off sc1
	s_waitcnt vmcnt(28)
	s_nop 0
	v_cvt_pk_f16_f32 v20, v44, v45
	v_cvt_pk_f16_f32 v21, v46, v47
	s_waitcnt vmcnt(27)
	v_cvt_pk_f16_f32 v22, v48, v49
	v_cvt_pk_f16_f32 v23, v50, v51
	global_store_dwordx4 v[58:59], v[20:23], off sc1
	s_waitcnt vmcnt(27)
	v_cvt_pk_f16_f32 v60, v60, v61
	v_cvt_pk_f16_f32 v61, v62, v63
	s_waitcnt vmcnt(26)
	v_cvt_pk_f16_f32 v62, v64, v65
	v_cvt_pk_f16_f32 v63, v66, v67
	global_store_dwordx4 v[92:93], v[60:63], off sc1
	s_waitcnt vmcnt(25)
	s_nop 0
	v_cvt_pk_f16_f32 v60, v72, v73
	v_cvt_pk_f16_f32 v61, v74, v75
	v_cvt_pk_f16_f32 v62, v68, v69
	v_cvt_pk_f16_f32 v63, v70, v71
	global_store_dwordx4 v[94:95], v[60:63], off sc1
	s_waitcnt vmcnt(25)
	s_nop 0
	v_cvt_pk_f16_f32 v60, v76, v77
	v_cvt_pk_f16_f32 v61, v78, v79
	s_waitcnt vmcnt(24)
	v_cvt_pk_f16_f32 v62, v80, v81
	v_cvt_pk_f16_f32 v63, v82, v83
	global_store_dwordx4 v[96:97], v[60:63], off sc1
	s_waitcnt vmcnt(24)
	s_nop 0
	v_cvt_pk_f16_f32 v60, v84, v85
	v_cvt_pk_f16_f32 v61, v86, v87
	s_waitcnt vmcnt(23)
	v_cvt_pk_f16_f32 v62, v88, v89
	v_cvt_pk_f16_f32 v63, v90, v91
	global_store_dwordx4 v[98:99], v[60:63], off sc1
	s_waitcnt vmcnt(23)
	v_cvt_pk_f16_f32 v100, v100, v101
	v_cvt_pk_f16_f32 v101, v102, v103
	s_waitcnt vmcnt(22)
	v_cvt_pk_f16_f32 v102, v104, v105
	v_cvt_pk_f16_f32 v103, v106, v107
	global_store_dwordx4 v[132:133], v[100:103], off sc1
	s_waitcnt vmcnt(21)
	s_nop 0
	v_cvt_pk_f16_f32 v100, v112, v113
	v_cvt_pk_f16_f32 v101, v114, v115
	v_cvt_pk_f16_f32 v102, v108, v109
	v_cvt_pk_f16_f32 v103, v110, v111
	global_store_dwordx4 v[134:135], v[100:103], off sc1
	s_waitcnt vmcnt(21)
	s_nop 0
	v_cvt_pk_f16_f32 v100, v116, v117
	v_cvt_pk_f16_f32 v101, v118, v119
	s_waitcnt vmcnt(20)
	v_cvt_pk_f16_f32 v102, v120, v121
	v_cvt_pk_f16_f32 v103, v122, v123
	global_store_dwordx4 v[136:137], v[100:103], off sc1
	s_waitcnt vmcnt(20)
	s_nop 0
	v_cvt_pk_f16_f32 v100, v124, v125
	v_cvt_pk_f16_f32 v101, v126, v127
	s_waitcnt vmcnt(19)
	v_cvt_pk_f16_f32 v102, v128, v129
	v_cvt_pk_f16_f32 v103, v130, v131
	global_store_dwordx4 v[138:139], v[100:103], off sc1
	s_waitcnt vmcnt(19)
	v_cvt_pk_f16_f32 v140, v140, v141
	v_cvt_pk_f16_f32 v141, v142, v143
	s_waitcnt vmcnt(18)
	v_cvt_pk_f16_f32 v142, v144, v145
	v_cvt_pk_f16_f32 v143, v146, v147
	global_store_dwordx4 v[172:173], v[140:143], off sc1
	s_waitcnt vmcnt(17)
	s_nop 0
	v_cvt_pk_f16_f32 v140, v152, v153
	v_cvt_pk_f16_f32 v141, v154, v155
	v_cvt_pk_f16_f32 v142, v148, v149
	v_cvt_pk_f16_f32 v143, v150, v151
	global_store_dwordx4 v[174:175], v[140:143], off sc1
	s_waitcnt vmcnt(17)
	s_nop 0
	v_cvt_pk_f16_f32 v140, v156, v157
	v_cvt_pk_f16_f32 v141, v158, v159
	s_waitcnt vmcnt(16)
	v_cvt_pk_f16_f32 v142, v160, v161
	v_cvt_pk_f16_f32 v143, v162, v163
	global_store_dwordx4 v[176:177], v[140:143], off sc1
	s_waitcnt vmcnt(16)
	s_nop 0
	v_cvt_pk_f16_f32 v140, v164, v165
	v_cvt_pk_f16_f32 v141, v166, v167
	s_waitcnt vmcnt(15)
	v_cvt_pk_f16_f32 v142, v168, v169
	v_cvt_pk_f16_f32 v143, v170, v171
	global_store_dwordx4 v[178:179], v[140:143], off sc1
